# ml_vectors: the three later gate loads of each mLSTM chunk unit issued together with the first (one round trip instead of three)
# speedup vs baseline: 1.0123x; 1.0123x over previous
; #define LAS __attribute__((address_space(3)))
; DI float log_sigmoid_f(float x) { return fminf(x, 0.f) - log1pf(__expf(-fabsf(x))); }
; DI void ml_vectors(Frame& F, int l, int t0, int h, LAS float* A, LAS float* IG, LAS float* RED) {
;     (void)RED;
;     if (F.wave == 0) {
;         const int s0 = 2 * F.lane; const float* gp = (const float*)(F.ws + WS_GATES) + (size_t)(t0 + s0) * 16; const float fb = inp(F, I_FB)[l * 4 + h], ib = inp(F, I_IB)[l * 4 + h];
;         float a0 = log_sigmoid_f(gp[12 + h] + fb), a1 = log_sigmoid_f(gp[16 + 12 + h] + fb);
;         IG[s0] = gp[8 + h] + ib; IG[s0 + 1] = gp[16 + 8 + h] + ib;
;         wscan2<false>(a0, a1, F.lane);
;         A[s0] = a0; A[s0 + 1] = a1; }
.LBB0_845:
	v_and_b32_e32 v0, -2, v1
	s_ashr_i32 s17, s16, 31
	s_lshl_b64 s[2:3], s[16:17], 7
	v_ashrrev_i32_e32 v1, 31, v0
	v_lshl_add_u64 v[0:1], s[2:3], 0, v[0:1]
	v_mov_b64_e32 v[4:5], s[24:25]
	v_mad_u64_u32 v[4:5], s[0:1], v0, s33, v[4:5]
	v_lshlrev_b32_e32 v0, 4, v132
	v_mad_i32_i24 v5, v1, s33, v5
	v_and_b32_e32 v2, 0x70, v0
	v_lshl_add_u64 v[0:1], v[4:5], 0, v[2:3]
	v_add_co_u32_e32 v8, vcc, s64, v0
	s_movk_i32 s0, 0x3000
	s_nop 0
	v_addc_co_u32_e32 v9, vcc, 0, v1, vcc
	v_add_co_u32_e32 v4, vcc, s0, v0
	s_mov_b64 s[0:1], 0
	s_nop 0
	v_addc_co_u32_e32 v5, vcc, 0, v1, vcc
	v_add_co_u32_e32 v0, vcc, s6, v0
	s_mov_b32 s7, s53
	s_nop 0
	v_addc_co_u32_e32 v1, vcc, 0, v1, vcc
	global_load_dwordx4 v[20:23], v[8:9], off offset:1536
	global_load_dwordx4 v[24:27], v[8:9], off offset:1664
	global_load_dwordx4 v[28:31], v[4:5], off
	global_load_dwordx4 v[32:35], v[4:5], off offset:128
	s_nop 0
	global_load_dwordx4 v[4:7], v[8:9], off offset:1024
	global_load_dwordx4 v[12:15], v[8:9], off offset:1152
	s_nop 0
	global_load_dwordx4 v[8:11], v[0:1], off offset:3584
	global_load_dwordx4 v[16:19], v[0:1], off offset:3712
	s_add_u32 s4, s20, s0
	v_and_b32_e32 v1, 63, v132
	v_readfirstlane_b32 s6, v132
	s_addc_u32 s5, s21, s1
	s_add_i32 s17, s19, s7
	v_lshlrev_b32_e32 v41, 2, v1
	s_cmp_gt_u32 s6, 63
	v_cmp_eq_u32_e32 vcc, 0, v1
	v_xor_b32_e32 v40, 0x80, v41
	s_cbranch_scc1 .LBB0_847
	v_lshl_or_b32 v36, v1, 1, s29
	v_ashrrev_i32_e32 v37, 31, v36
	v_lshlrev_b64 v[36:37], 6, v[36:37]
	v_lshl_add_u64 v[36:37], s[4:5], 0, v[36:37]
	s_mov_b64 s[0:1], 0x500000
	v_lshl_add_u64 v[36:37], v[36:37], 0, s[0:1]
	s_add_i32 s0, s17, 0x20870
	v_mov_b32_e32 v0, s0
	ds_read2_b32 v[38:39], v0 offset1:1
	s_lshl_b64 s[0:1], s[14:15], 2
	s_waitcnt lgkmcnt(0)
	v_readfirstlane_b32 s7, v38
	v_readfirstlane_b32 s19, v39
	s_add_u32 s20, s7, s0
	s_addc_u32 s21, s19, s1
	s_add_i32 s7, s17, 0x20868
	v_mov_b32_e32 v0, s7
	ds_read2_b32 v[42:43], v0 offset1:1
	global_load_dword v38, v3, s[20:21]
	s_waitcnt lgkmcnt(0)
	v_readfirstlane_b32 s7, v42
	v_readfirstlane_b32 s19, v43
	s_add_u32 s0, s7, s0
	s_addc_u32 s1, s19, s1
	global_load_dword v2, v3, s[0:1]
	global_load_dword v0, v[36:37], off offset:48
	global_load_dword v153, v[36:37], off offset:32
	global_load_dword v152, v[36:37], off offset:96
	global_load_dword v151, v[36:37], off offset:112
	s_waitcnt vmcnt(0)
	v_add_f32_e32 v0, v38, v0
	v_min_f32_e32 v39, 0, v0
	v_mul_f32_e64 v0, |v0|, s81
	v_exp_f32_e32 v0, v0
	s_nop 0
	v_add_f32_e32 v44, 1.0, v0
	v_add_f32_e32 v42, -1.0, v44
	v_sub_f32_e32 v43, v42, v44
	v_add_f32_e32 v43, 1.0, v43
	v_sub_f32_e32 v42, v0, v42
	v_add_f32_e32 v45, v42, v43
	v_frexp_mant_f32_e32 v42, v44
	v_cmp_gt_f32_e64 s[0:1], s87, v42
	v_cvt_f64_f32_e32 v[42:43], v44
	v_frexp_exp_i32_f64_e32 v42, v[42:43]
	v_subbrev_co_u32_e64 v42, s[0:1], 0, v42, s[0:1]
	v_sub_u32_e32 v43, 0, v42
	v_ldexp_f32 v44, v44, v43
	v_ldexp_f32 v43, v45, v43
	v_add_f32_e32 v45, -1.0, v44
	v_add_f32_e32 v46, 1.0, v45
	v_sub_f32_e32 v46, v44, v46
	v_add_f32_e32 v46, v43, v46
	v_add_f32_e32 v47, v45, v46
	v_sub_f32_e32 v45, v47, v45
	v_sub_f32_e32 v45, v46, v45
	v_add_f32_e32 v46, 1.0, v44
	v_add_f32_e32 v48, -1.0, v46
	v_sub_f32_e32 v44, v44, v48
	v_add_f32_e32 v43, v43, v44
	v_add_f32_e32 v44, v46, v43
	v_sub_f32_e32 v46, v44, v46
	v_sub_f32_e32 v43, v43, v46
	v_rcp_f32_e32 v46, v44
	v_cvt_f32_i32_e32 v42, v42
	v_cmp_neq_f32_e64 s[0:1], s82, v0
	v_mul_f32_e32 v48, v47, v46
	v_mul_f32_e32 v49, v44, v48
	v_fma_f32 v50, v48, v44, -v49
	v_fmac_f32_e32 v50, v48, v43
	v_add_f32_e32 v51, v49, v50
	v_sub_f32_e32 v52, v47, v51
	v_sub_f32_e32 v47, v47, v52
	v_sub_f32_e32 v49, v51, v49
	v_sub_f32_e32 v47, v47, v51
	v_add_f32_e32 v45, v45, v47
	v_sub_f32_e32 v47, v49, v50
	v_add_f32_e32 v45, v47, v45
	v_add_f32_e32 v47, v52, v45
	v_mul_f32_e32 v49, v46, v47
	v_mul_f32_e32 v50, v44, v49
	v_fma_f32 v44, v49, v44, -v50
	v_fmac_f32_e32 v44, v49, v43
	v_sub_f32_e32 v43, v52, v47
	v_add_f32_e32 v43, v45, v43
	v_add_f32_e32 v45, v50, v44
	v_sub_f32_e32 v51, v47, v45
	v_sub_f32_e32 v47, v47, v51
	v_sub_f32_e32 v50, v45, v50
	v_sub_f32_e32 v45, v47, v45
	v_add_f32_e32 v43, v43, v45
	v_sub_f32_e32 v44, v50, v44
	v_add_f32_e32 v43, v44, v43
	v_add_f32_e32 v44, v48, v49
	v_add_f32_e32 v43, v51, v43
	v_sub_f32_e32 v45, v44, v48
	v_mul_f32_e32 v43, v46, v43
	v_sub_f32_e32 v45, v49, v45
	v_add_f32_e32 v43, v45, v43
	v_mul_f32_e32 v48, 0x3f317218, v42
	v_add_f32_e32 v45, v44, v43
	v_fma_f32 v49, v42, s80, -v48
	v_mul_f32_e32 v46, v45, v45
	v_fmac_f32_e32 v49, 0xb102e308, v42
	v_sub_f32_e32 v42, v45, v44
	v_fmamk_f32 v47, v46, 0x3e9b6dac, v216
	v_sub_f32_e32 v42, v43, v42
	v_add_f32_e32 v43, v48, v49
	v_fmaak_f32 v47, v46, v47, 0x3f2aaada
	v_sub_f32_e32 v44, v43, v48
	v_ldexp_f32 v48, v45, 1
	v_mul_f32_e32 v45, v45, v46
	v_mul_f32_e32 v45, v45, v47
	v_add_f32_e32 v46, v48, v45
	v_sub_f32_e32 v47, v46, v48
	v_ldexp_f32 v42, v42, 1
	v_sub_f32_e32 v45, v45, v47
	v_add_f32_e32 v42, v42, v45
	v_add_f32_e32 v45, v46, v42
	v_sub_f32_e32 v46, v45, v46
	v_sub_f32_e32 v42, v42, v46
	v_add_f32_e32 v46, v43, v45
	v_sub_f32_e32 v47, v46, v43
	v_sub_f32_e32 v48, v46, v47
	v_sub_f32_e32 v44, v49, v44
	v_sub_f32_e32 v43, v43, v48
	v_sub_f32_e32 v45, v45, v47
	v_add_f32_e32 v43, v45, v43
	v_add_f32_e32 v45, v44, v42
	v_sub_f32_e32 v47, v45, v44
	v_sub_f32_e32 v48, v45, v47
	v_sub_f32_e32 v44, v44, v48
	v_sub_f32_e32 v42, v42, v47
	v_add_f32_e32 v43, v45, v43
	v_add_f32_e32 v42, v42, v44
	v_add_f32_e32 v44, v46, v43
	v_sub_f32_e32 v45, v44, v46
	v_sub_f32_e32 v43, v43, v45
	v_add_f32_e32 v42, v42, v43
	v_add_f32_e32 v42, v44, v42
; DI float log_sigmoid_f(float x) { return fminf(x, 0.f) - log1pf(__expf(-fabsf(x))); }
; DI float shup(float v, int o, int lane) { return __int_as_float(__builtin_amdgcn_ds_bpermute(((lane - o) & 63) << 2, __float_as_int(v))); }
; template <bool IS_MAX> DI void wscan2(float& x0, float& x1, int lane) {
;     x1 = IS_MAX ? fmaxf(x0, x1) : x0 + x1;
;     float s = x1;
; #pragma unroll
;     for (int o = 1; o < 64; o <<= 1) { const float y = shup(s, o, lane); if (lane >= o) s = IS_MAX ? fmaxf(s, y) : s + y; }
;     const float ex = shup(s, 1, lane);
;     if (lane > 0) { x0 = IS_MAX ? fmaxf(x0, ex) : x0 + ex; x1 = IS_MAX ? fmaxf(x1, ex) : x1 + ex; }
; }
; DI void ml_vectors(Frame& F, int l, int t0, int h, LAS float* A, LAS float* IG, LAS float* RED) {
;     ...
;         float a0 = log_sigmoid_f(gp[12 + h] + fb), a1 = log_sigmoid_f(gp[16 + 12 + h] + fb);
;         IG[s0] = gp[8 + h] + ib; IG[s0 + 1] = gp[16 + 8 + h] + ib;
;         wscan2<false>(a0, a1, F.lane);
;         A[s0] = a0; A[s0 + 1] = a1; }
	v_cndmask_b32_e64 v42, v230, v42, s[0:1]
	v_cmp_ngt_f32_e64 s[0:1], -1.0, v0
	s_nop 1
	v_cndmask_b32_e64 v42, v231, v42, s[0:1]
	v_cmp_neq_f32_e64 s[0:1], -1.0, v0
	s_nop 1
	v_cndmask_b32_e64 v42, v232, v42, s[0:1]
	v_cmp_lt_f32_e64 s[0:1], |v0|, s86
	s_nop 1
	v_cndmask_b32_e64 v0, v42, v0, s[0:1]
	v_sub_f32_e32 v42, v39, v0
	v_add_f32_e32 v0, v38, v151
	v_min_f32_e32 v43, 0, v0
	v_mul_f32_e64 v0, |v0|, s81
	v_exp_f32_e32 v0, v0
	s_nop 0
	v_add_f32_e32 v44, 1.0, v0
	v_add_f32_e32 v38, -1.0, v44
	v_sub_f32_e32 v39, v38, v44
	v_add_f32_e32 v39, 1.0, v39
	v_sub_f32_e32 v38, v0, v38
	v_add_f32_e32 v45, v38, v39
	v_frexp_mant_f32_e32 v38, v44
	v_cmp_gt_f32_e64 s[0:1], s87, v38
	v_cvt_f64_f32_e32 v[38:39], v44
	v_frexp_exp_i32_f64_e32 v38, v[38:39]
	v_subbrev_co_u32_e64 v38, s[0:1], 0, v38, s[0:1]
	v_sub_u32_e32 v39, 0, v38
	v_ldexp_f32 v44, v44, v39
	v_ldexp_f32 v39, v45, v39
	v_add_f32_e32 v45, -1.0, v44
	v_add_f32_e32 v46, 1.0, v45
	v_sub_f32_e32 v46, v44, v46
	v_add_f32_e32 v46, v39, v46
	v_add_f32_e32 v47, v45, v46
	v_sub_f32_e32 v45, v47, v45
	v_sub_f32_e32 v45, v46, v45
	v_add_f32_e32 v46, 1.0, v44
	v_add_f32_e32 v48, -1.0, v46
	v_sub_f32_e32 v44, v44, v48
	v_add_f32_e32 v39, v39, v44
	v_add_f32_e32 v44, v46, v39
	v_sub_f32_e32 v46, v44, v46
	v_sub_f32_e32 v39, v39, v46
	v_rcp_f32_e32 v46, v44
	v_cvt_f32_i32_e32 v38, v38
	v_cmp_neq_f32_e64 s[0:1], s82, v0
	v_mul_f32_e32 v48, v47, v46
	v_mul_f32_e32 v49, v44, v48
	v_fma_f32 v50, v48, v44, -v49
	v_fmac_f32_e32 v50, v48, v39
	v_add_f32_e32 v51, v49, v50
	v_sub_f32_e32 v52, v47, v51
	v_sub_f32_e32 v47, v47, v52
	v_sub_f32_e32 v49, v51, v49
	v_sub_f32_e32 v47, v47, v51
	v_add_f32_e32 v45, v45, v47
	v_sub_f32_e32 v47, v49, v50
	v_add_f32_e32 v45, v47, v45
	v_add_f32_e32 v47, v52, v45
	v_mul_f32_e32 v49, v46, v47
	v_mul_f32_e32 v50, v44, v49
	v_fma_f32 v44, v49, v44, -v50
	v_fmac_f32_e32 v44, v49, v39
	v_sub_f32_e32 v39, v52, v47
	v_add_f32_e32 v39, v45, v39
	v_add_f32_e32 v45, v50, v44
	v_sub_f32_e32 v51, v47, v45
	v_sub_f32_e32 v47, v47, v51
	v_sub_f32_e32 v50, v45, v50
	v_sub_f32_e32 v45, v47, v45
	v_add_f32_e32 v39, v39, v45
	v_sub_f32_e32 v44, v50, v44
	v_add_f32_e32 v39, v44, v39
	v_add_f32_e32 v44, v48, v49
	v_add_f32_e32 v39, v51, v39
	v_sub_f32_e32 v45, v44, v48
	v_mul_f32_e32 v39, v46, v39
	v_sub_f32_e32 v45, v49, v45
	v_add_f32_e32 v39, v45, v39
	v_mul_f32_e32 v48, 0x3f317218, v38
	v_add_f32_e32 v45, v44, v39
	v_fma_f32 v49, v38, s80, -v48
	v_mul_f32_e32 v46, v45, v45
	v_fmac_f32_e32 v49, 0xb102e308, v38
	v_sub_f32_e32 v38, v45, v44
	v_fmamk_f32 v47, v46, 0x3e9b6dac, v216
	v_sub_f32_e32 v38, v39, v38
	v_add_f32_e32 v39, v48, v49
	v_fmaak_f32 v47, v46, v47, 0x3f2aaada
	v_sub_f32_e32 v44, v39, v48
	v_ldexp_f32 v48, v45, 1
	v_mul_f32_e32 v45, v45, v46
	v_mul_f32_e32 v45, v45, v47
	v_add_f32_e32 v46, v48, v45
	v_sub_f32_e32 v47, v46, v48
	v_ldexp_f32 v38, v38, 1
	v_sub_f32_e32 v45, v45, v47
	v_add_f32_e32 v38, v38, v45
	v_add_f32_e32 v45, v46, v38
	v_sub_f32_e32 v46, v45, v46
	v_sub_f32_e32 v38, v38, v46
	v_add_f32_e32 v46, v39, v45
	v_sub_f32_e32 v47, v46, v39
	v_sub_f32_e32 v48, v46, v47
	v_sub_f32_e32 v44, v49, v44
	v_sub_f32_e32 v39, v39, v48
	v_sub_f32_e32 v45, v45, v47
	v_add_f32_e32 v39, v45, v39
	v_add_f32_e32 v45, v44, v38
	v_sub_f32_e32 v47, v45, v44
	v_sub_f32_e32 v48, v45, v47
	v_sub_f32_e32 v44, v44, v48
	v_sub_f32_e32 v38, v38, v47
	v_add_f32_e32 v39, v45, v39
	v_add_f32_e32 v38, v38, v44
	v_add_f32_e32 v44, v46, v39
	v_sub_f32_e32 v45, v44, v46
	v_sub_f32_e32 v39, v39, v45
	v_add_f32_e32 v38, v38, v39
	v_add_f32_e32 v38, v44, v38
	v_cndmask_b32_e64 v38, v230, v38, s[0:1]
	v_cmp_ngt_f32_e64 s[0:1], -1.0, v0
	v_mov_b32_e32 v39, v152
	s_nop 0
	v_cndmask_b32_e64 v38, v231, v38, s[0:1]
	v_cmp_neq_f32_e64 s[0:1], -1.0, v0
	s_nop 1
	v_cndmask_b32_e64 v38, v232, v38, s[0:1]
	v_cmp_lt_f32_e64 s[0:1], |v0|, s86
	s_nop 1
	v_cndmask_b32_e64 v0, v38, v0, s[0:1]
	v_mov_b32_e32 v38, v153
	v_sub_f32_e32 v44, v43, v0
	v_lshl_add_u32 v43, v1, 3, s17
	v_add_u32_e32 v45, 0x9b00, v43
	v_add_f32_e32 v0, v42, v44
	v_cmp_gt_u32_e64 s[0:1], 2, v1
	s_waitcnt vmcnt(0)
	v_pk_add_f32 v[36:37], v[2:3], v[38:39] op_sel_hi:[0,1]
	v_add_u32_e32 v2, 0xfc, v41
	v_and_b32_e32 v2, 0xfc, v2
	ds_write2_b32 v45, v36, v37 offset1:1
	ds_bpermute_b32 v36, v2, v0
	v_add_u32_e32 v37, 0xf8, v41
	v_and_b32_e32 v37, 0xfc, v37
	s_waitcnt lgkmcnt(0)
	v_add_f32_e32 v36, v0, v36
	v_cndmask_b32_e32 v36, v36, v0, vcc
	ds_bpermute_b32 v37, v37, v36
	s_waitcnt lgkmcnt(0)
	v_add_f32_e32 v37, v36, v37
	v_cndmask_b32_e64 v36, v37, v36, s[0:1]
	v_add_u32_e32 v37, 0xf0, v41
	v_and_b32_e32 v37, 0xfc, v37
	ds_bpermute_b32 v37, v37, v36
	v_cmp_gt_u32_e64 s[0:1], 4, v1
	s_waitcnt lgkmcnt(0)
	v_add_f32_e32 v37, v36, v37
	v_cndmask_b32_e64 v36, v37, v36, s[0:1]
	v_add_u32_e32 v37, 0xe0, v41
	v_and_b32_e32 v37, 0xfc, v37
	ds_bpermute_b32 v37, v37, v36
	v_cmp_gt_u32_e64 s[0:1], 8, v1
	s_waitcnt lgkmcnt(0)
	v_add_f32_e32 v37, v36, v37
	v_cndmask_b32_e64 v36, v37, v36, s[0:1]
	v_add_u32_e32 v37, 0xc0, v41
	v_and_b32_e32 v37, 0xfc, v37
	ds_bpermute_b32 v37, v37, v36
	v_cmp_gt_u32_e64 s[0:1], 16, v1
	s_waitcnt lgkmcnt(0)
	v_add_f32_e32 v37, v36, v37
	v_cndmask_b32_e64 v36, v37, v36, s[0:1]
	ds_bpermute_b32 v37, v40, v36
	v_cmp_gt_u32_e64 s[0:1], 32, v1
	s_waitcnt lgkmcnt(0)
	v_add_f32_e32 v37, v36, v37
	v_cndmask_b32_e64 v36, v37, v36, s[0:1]
	ds_bpermute_b32 v2, v2, v36
	s_waitcnt lgkmcnt(0)
	v_add_f32_e32 v36, v42, v2
	v_add_f32_e32 v2, v0, v2
	v_cndmask_b32_e32 v36, v36, v42, vcc
	v_cndmask_b32_e32 v0, v2, v0, vcc
	v_add_u32_e32 v2, 0x9900, v43
	ds_write2_b32 v2, v36, v0 offset1:1

; #define LAS __attribute__((address_space(3)))
; DI float log_sigmoid_f(float x) { return fminf(x, 0.f) - log1pf(__expf(-fabsf(x))); }
; DI void ml_vectors(Frame& F, int l, int t0, int h, LAS float* A, LAS float* IG, LAS float* RED) {
;     (void)RED;
;     if (F.wave == 0) {
;         const int s0 = 2 * F.lane; const float* gp = (const float*)(F.ws + WS_GATES) + (size_t)(t0 + s0) * 16; const float fb = inp(F, I_FB)[l * 4 + h], ib = inp(F, I_IB)[l * 4 + h];
;         float a0 = log_sigmoid_f(gp[12 + h] + fb), a1 = log_sigmoid_f(gp[16 + 12 + h] + fb);
;         IG[s0] = gp[8 + h] + ib; IG[s0 + 1] = gp[16 + 8 + h] + ib;
.LBB0_867:
	s_or_b64 exec, exec, s[0:1]
	v_ashrrev_i32_e32 v39, 31, v38
	v_lshl_add_u64 v[0:1], s[2:3], 0, v[38:39]
	v_mov_b64_e32 v[4:5], s[4:5]
	v_mad_u64_u32 v[4:5], s[0:1], v0, s33, v[4:5]
	v_mad_i32_i24 v5, v1, s33, v5
	v_lshlrev_b32_e32 v2, 1, v40
	v_lshl_add_u64 v[0:1], v[4:5], 0, v[2:3]
	s_mov_b32 s0, 0xb101000
	v_add_co_u32_e32 v4, vcc, s0, v0
	s_mov_b32 s0, 0xb103000
	s_nop 0
	v_addc_co_u32_e32 v5, vcc, 0, v1, vcc
	v_add_co_u32_e32 v8, vcc, s0, v0
	s_mov_b32 s0, 0xb102000
	s_nop 0
	v_addc_co_u32_e32 v9, vcc, 0, v1, vcc
	v_add_co_u32_e32 v0, vcc, s0, v0
	s_barrier
	global_load_dwordx4 v[20:23], v[4:5], off offset:1792
	s_nop 0
	global_load_dwordx4 v[4:7], v[4:5], off offset:1280
	v_addc_co_u32_e32 v1, vcc, 0, v1, vcc
	global_load_dwordx4 v[28:31], v[8:9], off offset:256
	s_nop 0
	global_load_dwordx4 v[8:11], v[0:1], off offset:3840
	s_mov_b64 s[0:1], 0
	s_mov_b32 s7, s53
	s_add_u32 s4, s4, s0
	v_and_b32_e32 v1, 63, v132
	v_readfirstlane_b32 s6, v132
	s_addc_u32 s5, s5, s1
	s_add_i32 s17, s17, s7
	v_lshlrev_b32_e32 v41, 2, v1
	s_cmp_gt_u32 s6, 63
	v_cmp_eq_u32_e32 vcc, 0, v1
	v_xor_b32_e32 v40, 0x80, v41
	s_cbranch_scc1 .LBB0_869
	s_add_i32 s0, s17, 0x20870
	v_mov_b32_e32 v0, s0
	ds_read2_b32 v[38:39], v0 offset1:1
	s_lshl_b64 s[0:1], s[14:15], 2
	v_lshl_or_b32 v36, v1, 1, s29
	v_ashrrev_i32_e32 v37, 31, v36
	v_lshlrev_b64 v[36:37], 6, v[36:37]
	s_waitcnt lgkmcnt(0)
	v_readfirstlane_b32 s7, v38
	v_readfirstlane_b32 s19, v39
	s_add_u32 s20, s7, s0
	s_addc_u32 s21, s19, s1
	s_add_i32 s7, s17, 0x20868
	v_mov_b32_e32 v0, s7
	ds_read2_b32 v[42:43], v0 offset1:1
	v_lshl_add_u64 v[36:37], s[4:5], 0, v[36:37]
	global_load_dword v38, v3, s[20:21] offset:4
	s_waitcnt lgkmcnt(0)
	v_readfirstlane_b32 s7, v42
	v_readfirstlane_b32 s19, v43
	s_add_u32 s0, s7, s0
	s_addc_u32 s1, s19, s1
	global_load_dword v2, v3, s[0:1] offset:4
	s_mov_b32 s0, 0x500000
	v_add_co_u32_e64 v36, s[0:1], s0, v36
	s_nop 1
	v_addc_co_u32_e64 v37, s[0:1], 0, v37, s[0:1]
	global_load_dword v0, v[36:37], off offset:52
	global_load_dword v153, v[36:37], off offset:36
	global_load_dword v152, v[36:37], off offset:100
	global_load_dword v151, v[36:37], off offset:116
	s_waitcnt vmcnt(0)
	v_add_f32_e32 v0, v38, v0
	v_min_f32_e32 v39, 0, v0
	v_mul_f32_e64 v0, |v0|, s81
	v_exp_f32_e32 v0, v0
	s_nop 0
	v_add_f32_e32 v44, 1.0, v0
	v_add_f32_e32 v42, -1.0, v44
	v_sub_f32_e32 v43, v42, v44
	v_add_f32_e32 v43, 1.0, v43
	v_sub_f32_e32 v42, v0, v42
	v_add_f32_e32 v45, v42, v43
	v_frexp_mant_f32_e32 v42, v44
	v_cmp_gt_f32_e64 s[0:1], s87, v42
	v_cvt_f64_f32_e32 v[42:43], v44
	v_frexp_exp_i32_f64_e32 v42, v[42:43]
	v_subbrev_co_u32_e64 v42, s[0:1], 0, v42, s[0:1]
	v_sub_u32_e32 v43, 0, v42
	v_ldexp_f32 v44, v44, v43
	v_ldexp_f32 v43, v45, v43
	v_add_f32_e32 v45, -1.0, v44
	v_add_f32_e32 v46, 1.0, v45
	v_sub_f32_e32 v46, v44, v46
	v_add_f32_e32 v46, v43, v46
	v_add_f32_e32 v47, v45, v46
	v_sub_f32_e32 v45, v47, v45
	v_sub_f32_e32 v45, v46, v45
	v_add_f32_e32 v46, 1.0, v44
	v_add_f32_e32 v48, -1.0, v46
	v_sub_f32_e32 v44, v44, v48
	v_add_f32_e32 v43, v43, v44
	v_add_f32_e32 v44, v46, v43
	v_sub_f32_e32 v46, v44, v46
	v_sub_f32_e32 v43, v43, v46
	v_rcp_f32_e32 v46, v44
	v_cvt_f32_i32_e32 v42, v42
	v_cmp_neq_f32_e64 s[0:1], s82, v0
	v_mul_f32_e32 v48, v47, v46
	v_mul_f32_e32 v49, v44, v48
	v_fma_f32 v50, v48, v44, -v49
	v_fmac_f32_e32 v50, v48, v43
	v_add_f32_e32 v51, v49, v50
	v_sub_f32_e32 v52, v47, v51
	v_sub_f32_e32 v47, v47, v52
	v_sub_f32_e32 v49, v51, v49
	v_sub_f32_e32 v47, v47, v51
	v_add_f32_e32 v45, v45, v47
	v_sub_f32_e32 v47, v49, v50
	v_add_f32_e32 v45, v47, v45
	v_add_f32_e32 v47, v52, v45
	v_mul_f32_e32 v49, v46, v47
	v_mul_f32_e32 v50, v44, v49
	v_fma_f32 v44, v49, v44, -v50
	v_fmac_f32_e32 v44, v49, v43
	v_sub_f32_e32 v43, v52, v47
	v_add_f32_e32 v43, v45, v43
	v_add_f32_e32 v45, v50, v44
	v_sub_f32_e32 v51, v47, v45
	v_sub_f32_e32 v47, v47, v51
	v_sub_f32_e32 v50, v45, v50
	v_sub_f32_e32 v45, v47, v45
	v_add_f32_e32 v43, v43, v45
	v_sub_f32_e32 v44, v50, v44
	v_add_f32_e32 v43, v44, v43
	v_add_f32_e32 v44, v48, v49
	v_add_f32_e32 v43, v51, v43
	v_sub_f32_e32 v45, v44, v48
	v_mul_f32_e32 v43, v46, v43
	v_sub_f32_e32 v45, v49, v45
	v_add_f32_e32 v43, v45, v43
	v_mul_f32_e32 v48, 0x3f317218, v42
	v_add_f32_e32 v45, v44, v43
	v_fma_f32 v49, v42, s80, -v48
	v_mul_f32_e32 v46, v45, v45
	v_fmac_f32_e32 v49, 0xb102e308, v42
	v_sub_f32_e32 v42, v45, v44
	v_fmamk_f32 v47, v46, 0x3e9b6dac, v216
	v_sub_f32_e32 v42, v43, v42
	v_add_f32_e32 v43, v48, v49
	v_fmaak_f32 v47, v46, v47, 0x3f2aaada
	v_sub_f32_e32 v44, v43, v48
	v_ldexp_f32 v48, v45, 1
	v_mul_f32_e32 v45, v45, v46
	v_mul_f32_e32 v45, v45, v47
	v_add_f32_e32 v46, v48, v45
	v_sub_f32_e32 v47, v46, v48
	v_ldexp_f32 v42, v42, 1
	v_sub_f32_e32 v45, v45, v47
	v_add_f32_e32 v42, v42, v45
	v_add_f32_e32 v45, v46, v42
	v_sub_f32_e32 v46, v45, v46
	v_sub_f32_e32 v42, v42, v46
	v_add_f32_e32 v46, v43, v45
	v_sub_f32_e32 v47, v46, v43
	v_sub_f32_e32 v48, v46, v47
	v_sub_f32_e32 v44, v49, v44
	v_sub_f32_e32 v43, v43, v48
	v_sub_f32_e32 v45, v45, v47
	v_add_f32_e32 v43, v45, v43
	v_add_f32_e32 v45, v44, v42
	v_sub_f32_e32 v47, v45, v44
	v_sub_f32_e32 v48, v45, v47
	v_sub_f32_e32 v44, v44, v48
	v_sub_f32_e32 v42, v42, v47
	v_add_f32_e32 v43, v45, v43
	v_add_f32_e32 v42, v42, v44
	v_add_f32_e32 v44, v46, v43
	v_sub_f32_e32 v45, v44, v46
	v_sub_f32_e32 v43, v43, v45
	v_add_f32_e32 v42, v42, v43
	v_add_f32_e32 v42, v44, v42
	v_cndmask_b32_e64 v42, v230, v42, s[0:1]
	v_cmp_ngt_f32_e64 s[0:1], -1.0, v0
; DI float log_sigmoid_f(float x) { return fminf(x, 0.f) - log1pf(__expf(-fabsf(x))); }
; DI float shup(float v, int o, int lane) { return __int_as_float(__builtin_amdgcn_ds_bpermute(((lane - o) & 63) << 2, __float_as_int(v))); }
; template <bool IS_MAX> DI void wscan2(float& x0, float& x1, int lane) {
;     x1 = IS_MAX ? fmaxf(x0, x1) : x0 + x1;
;     float s = x1;
; #pragma unroll
;     for (int o = 1; o < 64; o <<= 1) { const float y = shup(s, o, lane); if (lane >= o) s = IS_MAX ? fmaxf(s, y) : s + y; }
;     const float ex = shup(s, 1, lane);
;     if (lane > 0) { x0 = IS_MAX ? fmaxf(x0, ex) : x0 + ex; x1 = IS_MAX ? fmaxf(x1, ex) : x1 + ex; }
; }
; DI void ml_vectors(Frame& F, int l, int t0, int h, LAS float* A, LAS float* IG, LAS float* RED) {
;     ...
;         float a0 = log_sigmoid_f(gp[12 + h] + fb), a1 = log_sigmoid_f(gp[16 + 12 + h] + fb);
;         IG[s0] = gp[8 + h] + ib; IG[s0 + 1] = gp[16 + 8 + h] + ib;
;         wscan2<false>(a0, a1, F.lane);
;         A[s0] = a0; A[s0 + 1] = a1; }
	s_nop 1
	v_cndmask_b32_e64 v42, v231, v42, s[0:1]
	v_cmp_neq_f32_e64 s[0:1], -1.0, v0
	s_nop 1
	v_cndmask_b32_e64 v42, v232, v42, s[0:1]
	v_cmp_lt_f32_e64 s[0:1], |v0|, s86
	s_nop 1
	v_cndmask_b32_e64 v0, v42, v0, s[0:1]
	v_sub_f32_e32 v42, v39, v0
	v_add_f32_e32 v0, v38, v151
	v_min_f32_e32 v43, 0, v0
	v_mul_f32_e64 v0, |v0|, s81
	v_exp_f32_e32 v0, v0
	s_nop 0
	v_add_f32_e32 v44, 1.0, v0
	v_add_f32_e32 v38, -1.0, v44
	v_sub_f32_e32 v39, v38, v44
	v_add_f32_e32 v39, 1.0, v39
	v_sub_f32_e32 v38, v0, v38
	v_add_f32_e32 v45, v38, v39
	v_frexp_mant_f32_e32 v38, v44
	v_cmp_gt_f32_e64 s[0:1], s87, v38
	v_cvt_f64_f32_e32 v[38:39], v44
	v_frexp_exp_i32_f64_e32 v38, v[38:39]
	v_subbrev_co_u32_e64 v38, s[0:1], 0, v38, s[0:1]
	v_sub_u32_e32 v39, 0, v38
	v_ldexp_f32 v44, v44, v39
	v_ldexp_f32 v39, v45, v39
	v_add_f32_e32 v45, -1.0, v44
	v_add_f32_e32 v46, 1.0, v45
	v_sub_f32_e32 v46, v44, v46
	v_add_f32_e32 v46, v39, v46
	v_add_f32_e32 v47, v45, v46
	v_sub_f32_e32 v45, v47, v45
	v_sub_f32_e32 v45, v46, v45
	v_add_f32_e32 v46, 1.0, v44
	v_add_f32_e32 v48, -1.0, v46
	v_sub_f32_e32 v44, v44, v48
	v_add_f32_e32 v39, v39, v44
	v_add_f32_e32 v44, v46, v39
	v_sub_f32_e32 v46, v44, v46
	v_sub_f32_e32 v39, v39, v46
	v_rcp_f32_e32 v46, v44
	v_cvt_f32_i32_e32 v38, v38
	v_cmp_neq_f32_e64 s[0:1], s82, v0
	v_mul_f32_e32 v48, v47, v46
	v_mul_f32_e32 v49, v44, v48
	v_fma_f32 v50, v48, v44, -v49
	v_fmac_f32_e32 v50, v48, v39
	v_add_f32_e32 v51, v49, v50
	v_sub_f32_e32 v52, v47, v51
	v_sub_f32_e32 v47, v47, v52
	v_sub_f32_e32 v49, v51, v49
	v_sub_f32_e32 v47, v47, v51
	v_add_f32_e32 v45, v45, v47
	v_sub_f32_e32 v47, v49, v50
	v_add_f32_e32 v45, v47, v45
	v_add_f32_e32 v47, v52, v45
	v_mul_f32_e32 v49, v46, v47
	v_mul_f32_e32 v50, v44, v49
	v_fma_f32 v44, v49, v44, -v50
	v_fmac_f32_e32 v44, v49, v39
	v_sub_f32_e32 v39, v52, v47
	v_add_f32_e32 v39, v45, v39
	v_add_f32_e32 v45, v50, v44
	v_sub_f32_e32 v51, v47, v45
	v_sub_f32_e32 v47, v47, v51
	v_sub_f32_e32 v50, v45, v50
	v_sub_f32_e32 v45, v47, v45
	v_add_f32_e32 v39, v39, v45
	v_sub_f32_e32 v44, v50, v44
	v_add_f32_e32 v39, v44, v39
	v_add_f32_e32 v44, v48, v49
	v_add_f32_e32 v39, v51, v39
	v_sub_f32_e32 v45, v44, v48
	v_mul_f32_e32 v39, v46, v39
	v_sub_f32_e32 v45, v49, v45
	v_add_f32_e32 v39, v45, v39
	v_mul_f32_e32 v48, 0x3f317218, v38
	v_add_f32_e32 v45, v44, v39
	v_fma_f32 v49, v38, s80, -v48
	v_mul_f32_e32 v46, v45, v45
	v_fmac_f32_e32 v49, 0xb102e308, v38
	v_sub_f32_e32 v38, v45, v44
	v_fmamk_f32 v47, v46, 0x3e9b6dac, v216
	v_sub_f32_e32 v38, v39, v38
	v_add_f32_e32 v39, v48, v49
	v_fmaak_f32 v47, v46, v47, 0x3f2aaada
	v_sub_f32_e32 v44, v39, v48
	v_ldexp_f32 v48, v45, 1
	v_mul_f32_e32 v45, v45, v46
	v_mul_f32_e32 v45, v45, v47
	v_add_f32_e32 v46, v48, v45
	v_sub_f32_e32 v47, v46, v48
	v_ldexp_f32 v38, v38, 1
	v_sub_f32_e32 v45, v45, v47
	v_add_f32_e32 v38, v38, v45
	v_add_f32_e32 v45, v46, v38
	v_sub_f32_e32 v46, v45, v46
	v_sub_f32_e32 v38, v38, v46
	v_add_f32_e32 v46, v39, v45
	v_sub_f32_e32 v47, v46, v39
	v_sub_f32_e32 v48, v46, v47
	v_sub_f32_e32 v44, v49, v44
	v_sub_f32_e32 v39, v39, v48
	v_sub_f32_e32 v45, v45, v47
	v_add_f32_e32 v39, v45, v39
	v_add_f32_e32 v45, v44, v38
	v_sub_f32_e32 v47, v45, v44
	v_sub_f32_e32 v48, v45, v47
	v_sub_f32_e32 v44, v44, v48
	v_sub_f32_e32 v38, v38, v47
	v_add_f32_e32 v39, v45, v39
	v_add_f32_e32 v38, v38, v44
	v_add_f32_e32 v44, v46, v39
	v_sub_f32_e32 v45, v44, v46
	v_sub_f32_e32 v39, v39, v45
	v_add_f32_e32 v38, v38, v39
	v_add_f32_e32 v38, v44, v38
	v_cndmask_b32_e64 v38, v230, v38, s[0:1]
	v_cmp_ngt_f32_e64 s[0:1], -1.0, v0
	v_mov_b32_e32 v39, v152
	s_nop 0
	v_cndmask_b32_e64 v38, v231, v38, s[0:1]
	v_cmp_neq_f32_e64 s[0:1], -1.0, v0
	s_nop 1
	v_cndmask_b32_e64 v38, v232, v38, s[0:1]
	v_cmp_lt_f32_e64 s[0:1], |v0|, s86
	s_nop 1
	v_cndmask_b32_e64 v0, v38, v0, s[0:1]
	v_mov_b32_e32 v38, v153
	v_sub_f32_e32 v44, v43, v0
	v_lshl_add_u32 v43, v1, 3, s17
	v_add_u32_e32 v45, 0x9b00, v43
	v_add_f32_e32 v0, v42, v44
	v_cmp_gt_u32_e64 s[0:1], 2, v1
	s_waitcnt vmcnt(0)
	v_pk_add_f32 v[36:37], v[2:3], v[38:39] op_sel_hi:[0,1]
	v_add_u32_e32 v2, 0xfc, v41
	v_and_b32_e32 v2, 0xfc, v2
	ds_write2_b32 v45, v36, v37 offset1:1
	ds_bpermute_b32 v36, v2, v0
	v_add_u32_e32 v37, 0xf8, v41
	v_and_b32_e32 v37, 0xfc, v37
	s_waitcnt lgkmcnt(0)
	v_add_f32_e32 v36, v0, v36
	v_cndmask_b32_e32 v36, v36, v0, vcc
	ds_bpermute_b32 v37, v37, v36
	s_waitcnt lgkmcnt(0)
	v_add_f32_e32 v37, v36, v37
	v_cndmask_b32_e64 v36, v37, v36, s[0:1]
	v_add_u32_e32 v37, 0xf0, v41
	v_and_b32_e32 v37, 0xfc, v37
	ds_bpermute_b32 v37, v37, v36
	v_cmp_gt_u32_e64 s[0:1], 4, v1
	s_waitcnt lgkmcnt(0)
	v_add_f32_e32 v37, v36, v37
	v_cndmask_b32_e64 v36, v37, v36, s[0:1]
	v_add_u32_e32 v37, 0xe0, v41
	v_and_b32_e32 v37, 0xfc, v37
	ds_bpermute_b32 v37, v37, v36
	v_cmp_gt_u32_e64 s[0:1], 8, v1
	s_waitcnt lgkmcnt(0)
	v_add_f32_e32 v37, v36, v37
	v_cndmask_b32_e64 v36, v37, v36, s[0:1]
	v_add_u32_e32 v37, 0xc0, v41
	v_and_b32_e32 v37, 0xfc, v37
	ds_bpermute_b32 v37, v37, v36
	v_cmp_gt_u32_e64 s[0:1], 16, v1
	s_waitcnt lgkmcnt(0)
	v_add_f32_e32 v37, v36, v37
	v_cndmask_b32_e64 v36, v37, v36, s[0:1]
	ds_bpermute_b32 v37, v40, v36
	v_cmp_gt_u32_e64 s[0:1], 32, v1
	s_waitcnt lgkmcnt(0)
	v_add_f32_e32 v37, v36, v37
	v_cndmask_b32_e64 v36, v37, v36, s[0:1]
	ds_bpermute_b32 v2, v2, v36
	s_waitcnt lgkmcnt(0)
	v_add_f32_e32 v36, v42, v2
	v_add_f32_e32 v2, v0, v2
	v_cndmask_b32_e32 v36, v36, v42, vcc
	v_cndmask_b32_e32 v0, v2, v0, vcc
	v_add_u32_e32 v2, 0x9900, v43
	ds_write2_b32 v2, v36, v0 offset1:1

; #define LAS __attribute__((address_space(3)))
; DI float log_sigmoid_f(float x) { return fminf(x, 0.f) - log1pf(__expf(-fabsf(x))); }
; DI void ml_vectors(Frame& F, int l, int t0, int h, LAS float* A, LAS float* IG, LAS float* RED) {
;     (void)RED;
;     if (F.wave == 0) {
;         const int s0 = 2 * F.lane; const float* gp = (const float*)(F.ws + WS_GATES) + (size_t)(t0 + s0) * 16; const float fb = inp(F, I_FB)[l * 4 + h], ib = inp(F, I_IB)[l * 4 + h];
;         float a0 = log_sigmoid_f(gp[12 + h] + fb), a1 = log_sigmoid_f(gp[16 + 12 + h] + fb);
;         IG[s0] = gp[8 + h] + ib; IG[s0 + 1] = gp[16 + 8 + h] + ib;
.LBB0_889:
	s_or_b64 exec, exec, s[6:7]
	v_ashrrev_i32_e32 v39, 31, v38
	v_lshl_add_u64 v[0:1], s[2:3], 0, v[38:39]
	v_mov_b64_e32 v[12:13], s[4:5]
	v_mad_u64_u32 v[12:13], s[0:1], v0, s33, v[12:13]
	v_mad_i32_i24 v13, v1, s33, v13
	v_lshlrev_b32_e32 v2, 1, v40
	v_lshl_add_u64 v[0:1], v[12:13], 0, v[2:3]
	s_mov_b32 s0, 0xb101000
	v_add_co_u32_e32 v12, vcc, s0, v0
	s_mov_b32 s0, 0xb103000
	s_nop 0
	v_addc_co_u32_e32 v13, vcc, 0, v1, vcc
	v_add_co_u32_e32 v16, vcc, s0, v0
	s_mov_b32 s0, 0xb102000
	s_nop 0
	v_addc_co_u32_e32 v17, vcc, 0, v1, vcc
	v_add_co_u32_e32 v0, vcc, s0, v0
	s_barrier
	global_load_dwordx4 v[24:27], v[12:13], off offset:1920
	s_nop 0
	global_load_dwordx4 v[12:15], v[12:13], off offset:1408
	v_addc_co_u32_e32 v1, vcc, 0, v1, vcc
	global_load_dwordx4 v[32:35], v[16:17], off offset:384
	s_nop 0
	global_load_dwordx4 v[16:19], v[0:1], off offset:3968
	s_mov_b64 s[0:1], 0
	s_mov_b32 s7, s53
	s_add_u32 s2, s4, s0
	v_and_b32_e32 v1, 63, v132
	v_readfirstlane_b32 s6, v132
	s_addc_u32 s3, s5, s1
	s_add_i32 s17, s17, s7
	v_lshlrev_b32_e32 v41, 2, v1
	s_cmp_gt_u32 s6, 63
	v_cmp_eq_u32_e32 vcc, 0, v1
	v_xor_b32_e32 v40, 0x80, v41
	s_cbranch_scc1 .LBB0_891
	s_add_i32 s0, s17, 0x20870
	v_mov_b32_e32 v0, s0
	ds_read2_b32 v[38:39], v0 offset1:1
	s_lshl_b64 s[0:1], s[14:15], 2
	v_lshl_or_b32 v36, v1, 1, s29
	v_ashrrev_i32_e32 v37, 31, v36
	v_lshlrev_b64 v[36:37], 6, v[36:37]
	s_waitcnt lgkmcnt(0)
	v_readfirstlane_b32 s4, v38
	v_readfirstlane_b32 s5, v39
	s_add_u32 s4, s4, s0
	s_addc_u32 s5, s5, s1
	v_lshl_add_u64 v[36:37], s[2:3], 0, v[36:37]
	s_nop 1
	global_load_dword v38, v3, s[4:5] offset:8
	s_add_i32 s4, s17, 0x20868
	v_mov_b32_e32 v0, s4
	ds_read2_b32 v[42:43], v0 offset1:1
	s_waitcnt lgkmcnt(0)
	v_readfirstlane_b32 s4, v42
	v_readfirstlane_b32 s5, v43
	s_add_u32 s0, s4, s0
	s_addc_u32 s1, s5, s1
	global_load_dword v2, v3, s[0:1] offset:8
	s_mov_b32 s0, 0x500000
	v_add_co_u32_e64 v36, s[0:1], s0, v36
	s_nop 1
	v_addc_co_u32_e64 v37, s[0:1], 0, v37, s[0:1]
	global_load_dword v0, v[36:37], off offset:56
	global_load_dword v153, v[36:37], off offset:40
	global_load_dword v152, v[36:37], off offset:104
	global_load_dword v151, v[36:37], off offset:120
	s_waitcnt vmcnt(0)
	v_add_f32_e32 v0, v38, v0
	v_min_f32_e32 v39, 0, v0
	v_mul_f32_e64 v0, |v0|, s81
	v_exp_f32_e32 v0, v0
	s_nop 0
	v_add_f32_e32 v44, 1.0, v0
	v_add_f32_e32 v42, -1.0, v44
	v_sub_f32_e32 v43, v42, v44
	v_add_f32_e32 v43, 1.0, v43
	v_sub_f32_e32 v42, v0, v42
	v_add_f32_e32 v45, v42, v43
	v_frexp_mant_f32_e32 v42, v44
	v_cmp_gt_f32_e64 s[0:1], s87, v42
	v_cvt_f64_f32_e32 v[42:43], v44
	v_frexp_exp_i32_f64_e32 v42, v[42:43]
	v_subbrev_co_u32_e64 v42, s[0:1], 0, v42, s[0:1]
	v_sub_u32_e32 v43, 0, v42
	v_ldexp_f32 v44, v44, v43
	v_ldexp_f32 v43, v45, v43
	v_add_f32_e32 v45, -1.0, v44
	v_add_f32_e32 v46, 1.0, v45
	v_sub_f32_e32 v46, v44, v46
	v_add_f32_e32 v46, v43, v46
	v_add_f32_e32 v47, v45, v46
	v_sub_f32_e32 v45, v47, v45
	v_sub_f32_e32 v45, v46, v45
	v_add_f32_e32 v46, 1.0, v44
	v_add_f32_e32 v48, -1.0, v46
	v_sub_f32_e32 v44, v44, v48
	v_add_f32_e32 v43, v43, v44
	v_add_f32_e32 v44, v46, v43
	v_sub_f32_e32 v46, v44, v46
	v_sub_f32_e32 v43, v43, v46
	v_rcp_f32_e32 v46, v44
	v_cvt_f32_i32_e32 v42, v42
	v_cmp_neq_f32_e64 s[0:1], s82, v0
	v_mul_f32_e32 v48, v47, v46
	v_mul_f32_e32 v49, v44, v48
	v_fma_f32 v50, v48, v44, -v49
	v_fmac_f32_e32 v50, v48, v43
	v_add_f32_e32 v51, v49, v50
	v_sub_f32_e32 v52, v47, v51
	v_sub_f32_e32 v47, v47, v52
	v_sub_f32_e32 v49, v51, v49
	v_sub_f32_e32 v47, v47, v51
	v_add_f32_e32 v45, v45, v47
	v_sub_f32_e32 v47, v49, v50
	v_add_f32_e32 v45, v47, v45
	v_add_f32_e32 v47, v52, v45
	v_mul_f32_e32 v49, v46, v47
	v_mul_f32_e32 v50, v44, v49
	v_fma_f32 v44, v49, v44, -v50
	v_fmac_f32_e32 v44, v49, v43
	v_sub_f32_e32 v43, v52, v47
	v_add_f32_e32 v43, v45, v43
	v_add_f32_e32 v45, v50, v44
	v_sub_f32_e32 v51, v47, v45
	v_sub_f32_e32 v47, v47, v51
	v_sub_f32_e32 v50, v45, v50
	v_sub_f32_e32 v45, v47, v45
	v_add_f32_e32 v43, v43, v45
	v_sub_f32_e32 v44, v50, v44
	v_add_f32_e32 v43, v44, v43
	v_add_f32_e32 v44, v48, v49
	v_add_f32_e32 v43, v51, v43
	v_sub_f32_e32 v45, v44, v48
	v_mul_f32_e32 v43, v46, v43
	v_sub_f32_e32 v45, v49, v45
	v_add_f32_e32 v43, v45, v43
	v_mul_f32_e32 v48, 0x3f317218, v42
	v_add_f32_e32 v45, v44, v43
	v_fma_f32 v49, v42, s80, -v48
	v_mul_f32_e32 v46, v45, v45
	v_fmac_f32_e32 v49, 0xb102e308, v42
	v_sub_f32_e32 v42, v45, v44
	v_fmamk_f32 v47, v46, 0x3e9b6dac, v216
	v_sub_f32_e32 v42, v43, v42
	v_add_f32_e32 v43, v48, v49
	v_fmaak_f32 v47, v46, v47, 0x3f2aaada
	v_sub_f32_e32 v44, v43, v48
	v_ldexp_f32 v48, v45, 1
	v_mul_f32_e32 v45, v45, v46
	v_mul_f32_e32 v45, v45, v47
	v_add_f32_e32 v46, v48, v45
	v_sub_f32_e32 v47, v46, v48
	v_ldexp_f32 v42, v42, 1
	v_sub_f32_e32 v45, v45, v47
	v_add_f32_e32 v42, v42, v45
	v_add_f32_e32 v45, v46, v42
	v_sub_f32_e32 v46, v45, v46
	v_sub_f32_e32 v42, v42, v46
	v_add_f32_e32 v46, v43, v45
	v_sub_f32_e32 v47, v46, v43
	v_sub_f32_e32 v48, v46, v47
	v_sub_f32_e32 v44, v49, v44
	v_sub_f32_e32 v43, v43, v48
	v_sub_f32_e32 v45, v45, v47
	v_add_f32_e32 v43, v45, v43
	v_add_f32_e32 v45, v44, v42
	v_sub_f32_e32 v47, v45, v44
	v_sub_f32_e32 v48, v45, v47
	v_sub_f32_e32 v44, v44, v48
	v_sub_f32_e32 v42, v42, v47
	v_add_f32_e32 v43, v45, v43
	v_add_f32_e32 v42, v42, v44
	v_add_f32_e32 v44, v46, v43
	v_sub_f32_e32 v45, v44, v46
	v_sub_f32_e32 v43, v43, v45
	v_add_f32_e32 v42, v42, v43
	v_add_f32_e32 v42, v44, v42
	v_cndmask_b32_e64 v42, v230, v42, s[0:1]
	v_cmp_ngt_f32_e64 s[0:1], -1.0, v0
; DI float log_sigmoid_f(float x) { return fminf(x, 0.f) - log1pf(__expf(-fabsf(x))); }
; DI float shup(float v, int o, int lane) { return __int_as_float(__builtin_amdgcn_ds_bpermute(((lane - o) & 63) << 2, __float_as_int(v))); }
; template <bool IS_MAX> DI void wscan2(float& x0, float& x1, int lane) {
;     x1 = IS_MAX ? fmaxf(x0, x1) : x0 + x1;
;     float s = x1;
; #pragma unroll
;     for (int o = 1; o < 64; o <<= 1) { const float y = shup(s, o, lane); if (lane >= o) s = IS_MAX ? fmaxf(s, y) : s + y; }
;     const float ex = shup(s, 1, lane);
;     if (lane > 0) { x0 = IS_MAX ? fmaxf(x0, ex) : x0 + ex; x1 = IS_MAX ? fmaxf(x1, ex) : x1 + ex; }
; }
; DI void ml_vectors(Frame& F, int l, int t0, int h, LAS float* A, LAS float* IG, LAS float* RED) {
;     ...
;         float a0 = log_sigmoid_f(gp[12 + h] + fb), a1 = log_sigmoid_f(gp[16 + 12 + h] + fb);
;         IG[s0] = gp[8 + h] + ib; IG[s0 + 1] = gp[16 + 8 + h] + ib;
;         wscan2<false>(a0, a1, F.lane);
;         A[s0] = a0; A[s0 + 1] = a1; }
	s_nop 1
	v_cndmask_b32_e64 v42, v231, v42, s[0:1]
	v_cmp_neq_f32_e64 s[0:1], -1.0, v0
	s_nop 1
	v_cndmask_b32_e64 v42, v232, v42, s[0:1]
	v_cmp_lt_f32_e64 s[0:1], |v0|, s86
	s_nop 1
	v_cndmask_b32_e64 v0, v42, v0, s[0:1]
	v_sub_f32_e32 v42, v39, v0
	v_add_f32_e32 v0, v38, v151
	v_min_f32_e32 v43, 0, v0
	v_mul_f32_e64 v0, |v0|, s81
	v_exp_f32_e32 v0, v0
	s_nop 0
	v_add_f32_e32 v44, 1.0, v0
	v_add_f32_e32 v38, -1.0, v44
	v_sub_f32_e32 v39, v38, v44
	v_add_f32_e32 v39, 1.0, v39
	v_sub_f32_e32 v38, v0, v38
	v_add_f32_e32 v45, v38, v39
	v_frexp_mant_f32_e32 v38, v44
	v_cmp_gt_f32_e64 s[0:1], s87, v38
	v_cvt_f64_f32_e32 v[38:39], v44
	v_frexp_exp_i32_f64_e32 v38, v[38:39]
	v_subbrev_co_u32_e64 v38, s[0:1], 0, v38, s[0:1]
	v_sub_u32_e32 v39, 0, v38
	v_ldexp_f32 v44, v44, v39
	v_ldexp_f32 v39, v45, v39
	v_add_f32_e32 v45, -1.0, v44
	v_add_f32_e32 v46, 1.0, v45
	v_sub_f32_e32 v46, v44, v46
	v_add_f32_e32 v46, v39, v46
	v_add_f32_e32 v47, v45, v46
	v_sub_f32_e32 v45, v47, v45
	v_sub_f32_e32 v45, v46, v45
	v_add_f32_e32 v46, 1.0, v44
	v_add_f32_e32 v48, -1.0, v46
	v_sub_f32_e32 v44, v44, v48
	v_add_f32_e32 v39, v39, v44
	v_add_f32_e32 v44, v46, v39
	v_sub_f32_e32 v46, v44, v46
	v_sub_f32_e32 v39, v39, v46
	v_rcp_f32_e32 v46, v44
	v_cvt_f32_i32_e32 v38, v38
	v_cmp_neq_f32_e64 s[0:1], s82, v0
	v_mul_f32_e32 v48, v47, v46
	v_mul_f32_e32 v49, v44, v48
	v_fma_f32 v50, v48, v44, -v49
	v_fmac_f32_e32 v50, v48, v39
	v_add_f32_e32 v51, v49, v50
	v_sub_f32_e32 v52, v47, v51
	v_sub_f32_e32 v47, v47, v52
	v_sub_f32_e32 v49, v51, v49
	v_sub_f32_e32 v47, v47, v51
	v_add_f32_e32 v45, v45, v47
	v_sub_f32_e32 v47, v49, v50
	v_add_f32_e32 v45, v47, v45
	v_add_f32_e32 v47, v52, v45
	v_mul_f32_e32 v49, v46, v47
	v_mul_f32_e32 v50, v44, v49
	v_fma_f32 v44, v49, v44, -v50
	v_fmac_f32_e32 v44, v49, v39
	v_sub_f32_e32 v39, v52, v47
	v_add_f32_e32 v39, v45, v39
	v_add_f32_e32 v45, v50, v44
	v_sub_f32_e32 v51, v47, v45
	v_sub_f32_e32 v47, v47, v51
	v_sub_f32_e32 v50, v45, v50
	v_sub_f32_e32 v45, v47, v45
	v_add_f32_e32 v39, v39, v45
	v_sub_f32_e32 v44, v50, v44
	v_add_f32_e32 v39, v44, v39
	v_add_f32_e32 v44, v48, v49
	v_add_f32_e32 v39, v51, v39
	v_sub_f32_e32 v45, v44, v48
	v_mul_f32_e32 v39, v46, v39
	v_sub_f32_e32 v45, v49, v45
	v_add_f32_e32 v39, v45, v39
	v_mul_f32_e32 v48, 0x3f317218, v38
	v_add_f32_e32 v45, v44, v39
	v_fma_f32 v49, v38, s80, -v48
	v_mul_f32_e32 v46, v45, v45
	v_fmac_f32_e32 v49, 0xb102e308, v38
	v_sub_f32_e32 v38, v45, v44
	v_fmamk_f32 v47, v46, 0x3e9b6dac, v216
	v_sub_f32_e32 v38, v39, v38
	v_add_f32_e32 v39, v48, v49
	v_fmaak_f32 v47, v46, v47, 0x3f2aaada
	v_sub_f32_e32 v44, v39, v48
	v_ldexp_f32 v48, v45, 1
	v_mul_f32_e32 v45, v45, v46
	v_mul_f32_e32 v45, v45, v47
	v_add_f32_e32 v46, v48, v45
	v_sub_f32_e32 v47, v46, v48
	v_ldexp_f32 v38, v38, 1
	v_sub_f32_e32 v45, v45, v47
	v_add_f32_e32 v38, v38, v45
	v_add_f32_e32 v45, v46, v38
	v_sub_f32_e32 v46, v45, v46
	v_sub_f32_e32 v38, v38, v46
	v_add_f32_e32 v46, v39, v45
	v_sub_f32_e32 v47, v46, v39
	v_sub_f32_e32 v48, v46, v47
	v_sub_f32_e32 v44, v49, v44
	v_sub_f32_e32 v39, v39, v48
	v_sub_f32_e32 v45, v45, v47
	v_add_f32_e32 v39, v45, v39
	v_add_f32_e32 v45, v44, v38
	v_sub_f32_e32 v47, v45, v44
	v_sub_f32_e32 v48, v45, v47
	v_sub_f32_e32 v44, v44, v48
	v_sub_f32_e32 v38, v38, v47
	v_add_f32_e32 v39, v45, v39
	v_add_f32_e32 v38, v38, v44
	v_add_f32_e32 v44, v46, v39
	v_sub_f32_e32 v45, v44, v46
	v_sub_f32_e32 v39, v39, v45
	v_add_f32_e32 v38, v38, v39
	v_add_f32_e32 v38, v44, v38
	v_cndmask_b32_e64 v38, v230, v38, s[0:1]
	v_cmp_ngt_f32_e64 s[0:1], -1.0, v0
	v_mov_b32_e32 v39, v152
	s_nop 0
	v_cndmask_b32_e64 v38, v231, v38, s[0:1]
	v_cmp_neq_f32_e64 s[0:1], -1.0, v0
	s_nop 1
	v_cndmask_b32_e64 v38, v232, v38, s[0:1]
	v_cmp_lt_f32_e64 s[0:1], |v0|, s86
	s_nop 1
	v_cndmask_b32_e64 v0, v38, v0, s[0:1]
	v_mov_b32_e32 v38, v153
	v_sub_f32_e32 v44, v43, v0
	v_lshl_add_u32 v43, v1, 3, s17
	v_add_u32_e32 v45, 0x9b00, v43
	v_add_f32_e32 v0, v42, v44
	v_cmp_gt_u32_e64 s[0:1], 2, v1
	s_waitcnt vmcnt(0)
	v_pk_add_f32 v[36:37], v[2:3], v[38:39] op_sel_hi:[0,1]
	v_add_u32_e32 v2, 0xfc, v41
	v_and_b32_e32 v2, 0xfc, v2
	ds_write2_b32 v45, v36, v37 offset1:1
	ds_bpermute_b32 v36, v2, v0
	v_add_u32_e32 v37, 0xf8, v41
	v_and_b32_e32 v37, 0xfc, v37
	s_waitcnt lgkmcnt(0)
	v_add_f32_e32 v36, v0, v36
	v_cndmask_b32_e32 v36, v36, v0, vcc
	ds_bpermute_b32 v37, v37, v36
	s_waitcnt lgkmcnt(0)
	v_add_f32_e32 v37, v36, v37
	v_cndmask_b32_e64 v36, v37, v36, s[0:1]
	v_add_u32_e32 v37, 0xf0, v41
	v_and_b32_e32 v37, 0xfc, v37
	ds_bpermute_b32 v37, v37, v36
	v_cmp_gt_u32_e64 s[0:1], 4, v1
	s_waitcnt lgkmcnt(0)
	v_add_f32_e32 v37, v36, v37
	v_cndmask_b32_e64 v36, v37, v36, s[0:1]
	v_add_u32_e32 v37, 0xe0, v41
	v_and_b32_e32 v37, 0xfc, v37
	ds_bpermute_b32 v37, v37, v36
	v_cmp_gt_u32_e64 s[0:1], 8, v1
	s_waitcnt lgkmcnt(0)
	v_add_f32_e32 v37, v36, v37
	v_cndmask_b32_e64 v36, v37, v36, s[0:1]
	v_add_u32_e32 v37, 0xc0, v41
	v_and_b32_e32 v37, 0xfc, v37
	ds_bpermute_b32 v37, v37, v36
	v_cmp_gt_u32_e64 s[0:1], 16, v1
	s_waitcnt lgkmcnt(0)
	v_add_f32_e32 v37, v36, v37
	v_cndmask_b32_e64 v36, v37, v36, s[0:1]
	ds_bpermute_b32 v37, v40, v36
	v_cmp_gt_u32_e64 s[0:1], 32, v1
	s_waitcnt lgkmcnt(0)
	v_add_f32_e32 v37, v36, v37
	v_cndmask_b32_e64 v36, v37, v36, s[0:1]
	ds_bpermute_b32 v2, v2, v36
	s_waitcnt lgkmcnt(0)
	v_add_f32_e32 v36, v42, v2
	v_add_f32_e32 v2, v0, v2
	v_cndmask_b32_e32 v36, v36, v42, vcc
	v_cndmask_b32_e32 v0, v2, v0, vcc
	v_add_u32_e32 v2, 0x9900, v43
	ds_write2_b32 v2, v36, v0 offset1:1

; #define LAS __attribute__((address_space(3)))
; DI float log_sigmoid_f(float x) { return fminf(x, 0.f) - log1pf(__expf(-fabsf(x))); }
; DI void ml_vectors(Frame& F, int l, int t0, int h, LAS float* A, LAS float* IG, LAS float* RED) {
;     (void)RED;
;     if (F.wave == 0) {
;         const int s0 = 2 * F.lane; const float* gp = (const float*)(F.ws + WS_GATES) + (size_t)(t0 + s0) * 16; const float fb = inp(F, I_FB)[l * 4 + h], ib = inp(F, I_IB)[l * 4 + h];
;         float a0 = log_sigmoid_f(gp[12 + h] + fb), a1 = log_sigmoid_f(gp[16 + 12 + h] + fb);
;         IG[s0] = gp[8 + h] + ib; IG[s0 + 1] = gp[16 + 8 + h] + ib;
.LBB0_911:
	s_or_b64 exec, exec, s[4:5]
	s_mov_b64 s[0:1], 0
	s_mov_b32 s5, s53
	s_barrier
	s_add_u32 s20, s2, s0
	v_and_b32_e32 v1, 63, v132
	v_readfirstlane_b32 s4, v132
	s_addc_u32 s21, s3, s1
	s_add_i32 s17, s17, s5
	v_lshlrev_b32_e32 v9, 2, v1
	s_cmp_gt_u32 s4, 63
	v_cmp_eq_u32_e32 vcc, 0, v1
	v_xor_b32_e32 v8, 0x80, v9
	s_cbranch_scc1 .LBB0_913
	s_add_i32 s0, s17, 0x20870
	v_mov_b32_e32 v0, s0
	ds_read2_b32 v[6:7], v0 offset1:1
	s_lshl_b64 s[0:1], s[14:15], 2
	v_lshl_or_b32 v4, v1, 1, s29
	v_ashrrev_i32_e32 v5, 31, v4
	v_lshlrev_b64 v[4:5], 6, v[4:5]
	s_waitcnt lgkmcnt(0)
	v_readfirstlane_b32 s2, v6
	v_readfirstlane_b32 s3, v7
	s_add_u32 s2, s2, s0
	s_addc_u32 s3, s3, s1
	v_lshl_add_u64 v[4:5], s[20:21], 0, v[4:5]
	s_nop 1
	global_load_dword v6, v3, s[2:3] offset:12
	s_add_i32 s2, s17, 0x20868
	v_mov_b32_e32 v0, s2
	ds_read2_b32 v[10:11], v0 offset1:1
	s_waitcnt lgkmcnt(0)
	v_readfirstlane_b32 s2, v10
	v_readfirstlane_b32 s3, v11
	s_add_u32 s0, s2, s0
	s_addc_u32 s1, s3, s1
	global_load_dword v2, v3, s[0:1] offset:12
	s_mov_b32 s0, 0x500000
	v_add_co_u32_e64 v4, s[0:1], s0, v4
	s_nop 1
	v_addc_co_u32_e64 v5, s[0:1], 0, v5, s[0:1]
	global_load_dword v0, v[4:5], off offset:60
	global_load_dword v153, v[4:5], off offset:44
	global_load_dword v152, v[4:5], off offset:108
	global_load_dword v151, v[4:5], off offset:124
	s_waitcnt vmcnt(0)
	v_add_f32_e32 v0, v6, v0
	v_min_f32_e32 v7, 0, v0
	v_mul_f32_e64 v0, |v0|, s81
	v_exp_f32_e32 v0, v0
	s_nop 0
	v_add_f32_e32 v20, 1.0, v0
	v_add_f32_e32 v10, -1.0, v20
	v_sub_f32_e32 v11, v10, v20
	v_add_f32_e32 v11, 1.0, v11
	v_sub_f32_e32 v10, v0, v10
	v_add_f32_e32 v21, v10, v11
	v_frexp_mant_f32_e32 v10, v20
	v_cmp_gt_f32_e64 s[0:1], s87, v10
	v_cvt_f64_f32_e32 v[10:11], v20
	v_frexp_exp_i32_f64_e32 v10, v[10:11]
	v_subbrev_co_u32_e64 v10, s[0:1], 0, v10, s[0:1]
	v_sub_u32_e32 v11, 0, v10
	v_ldexp_f32 v20, v20, v11
	v_ldexp_f32 v11, v21, v11
	v_add_f32_e32 v21, -1.0, v20
	v_add_f32_e32 v22, 1.0, v21
	v_sub_f32_e32 v22, v20, v22
	v_add_f32_e32 v22, v11, v22
	v_add_f32_e32 v23, v21, v22
	v_sub_f32_e32 v21, v23, v21
	v_sub_f32_e32 v21, v22, v21
	v_add_f32_e32 v22, 1.0, v20
	v_add_f32_e32 v28, -1.0, v22
	v_sub_f32_e32 v20, v20, v28
	v_add_f32_e32 v11, v11, v20
	v_add_f32_e32 v20, v22, v11
	v_sub_f32_e32 v22, v20, v22
	v_sub_f32_e32 v11, v11, v22
	v_rcp_f32_e32 v22, v20
	v_cvt_f32_i32_e32 v10, v10
	v_cmp_neq_f32_e64 s[0:1], s82, v0
	v_mul_f32_e32 v28, v23, v22
	v_mul_f32_e32 v29, v20, v28
	v_fma_f32 v30, v28, v20, -v29
	v_fmac_f32_e32 v30, v28, v11
	v_add_f32_e32 v31, v29, v30
	v_sub_f32_e32 v36, v23, v31
	v_sub_f32_e32 v23, v23, v36
	v_sub_f32_e32 v29, v31, v29
	v_sub_f32_e32 v23, v23, v31
	v_add_f32_e32 v21, v21, v23
	v_sub_f32_e32 v23, v29, v30
	v_add_f32_e32 v21, v23, v21
	v_add_f32_e32 v23, v36, v21
	v_mul_f32_e32 v29, v22, v23
	v_mul_f32_e32 v30, v20, v29
	v_fma_f32 v20, v29, v20, -v30
	v_fmac_f32_e32 v20, v29, v11
	v_sub_f32_e32 v11, v36, v23
	v_add_f32_e32 v11, v21, v11
	v_add_f32_e32 v21, v30, v20
	v_sub_f32_e32 v31, v23, v21
	v_sub_f32_e32 v23, v23, v31
	v_sub_f32_e32 v30, v21, v30
	v_sub_f32_e32 v21, v23, v21
	v_add_f32_e32 v11, v11, v21
	v_sub_f32_e32 v20, v30, v20
	v_add_f32_e32 v11, v20, v11
	v_add_f32_e32 v20, v28, v29
	v_add_f32_e32 v11, v31, v11
	v_sub_f32_e32 v21, v20, v28
	v_mul_f32_e32 v11, v22, v11
	v_sub_f32_e32 v21, v29, v21
	v_add_f32_e32 v11, v21, v11
	v_mul_f32_e32 v28, 0x3f317218, v10
	v_add_f32_e32 v21, v20, v11
	v_fma_f32 v29, v10, s80, -v28
	v_mul_f32_e32 v22, v21, v21
	v_fmac_f32_e32 v29, 0xb102e308, v10
	v_sub_f32_e32 v10, v21, v20
	v_fmamk_f32 v23, v22, 0x3e9b6dac, v216
	v_sub_f32_e32 v10, v11, v10
	v_add_f32_e32 v11, v28, v29
	v_fmaak_f32 v23, v22, v23, 0x3f2aaada
	v_sub_f32_e32 v20, v11, v28
	v_ldexp_f32 v28, v21, 1
	v_mul_f32_e32 v21, v21, v22
	v_mul_f32_e32 v21, v21, v23
	v_add_f32_e32 v22, v28, v21
	v_sub_f32_e32 v23, v22, v28
	v_ldexp_f32 v10, v10, 1
	v_sub_f32_e32 v21, v21, v23
	v_add_f32_e32 v10, v10, v21
	v_add_f32_e32 v21, v22, v10
	v_sub_f32_e32 v22, v21, v22
	v_sub_f32_e32 v10, v10, v22
	v_add_f32_e32 v22, v11, v21
	v_sub_f32_e32 v23, v22, v11
	v_sub_f32_e32 v28, v22, v23
	v_sub_f32_e32 v20, v29, v20
	v_sub_f32_e32 v11, v11, v28
	v_sub_f32_e32 v21, v21, v23
	v_add_f32_e32 v11, v21, v11
	v_add_f32_e32 v21, v20, v10
	v_sub_f32_e32 v23, v21, v20
	v_sub_f32_e32 v28, v21, v23
	v_sub_f32_e32 v20, v20, v28
	v_sub_f32_e32 v10, v10, v23
	v_add_f32_e32 v11, v21, v11
	v_add_f32_e32 v10, v10, v20
	v_add_f32_e32 v20, v22, v11
	v_sub_f32_e32 v21, v20, v22
	v_sub_f32_e32 v11, v11, v21
	v_add_f32_e32 v10, v10, v11
	v_add_f32_e32 v10, v20, v10
	v_cndmask_b32_e64 v10, v230, v10, s[0:1]
	v_cmp_ngt_f32_e64 s[0:1], -1.0, v0
	s_nop 1
	v_cndmask_b32_e64 v10, v231, v10, s[0:1]
	v_cmp_neq_f32_e64 s[0:1], -1.0, v0
	s_nop 1
	v_cndmask_b32_e64 v10, v232, v10, s[0:1]
	v_cmp_lt_f32_e64 s[0:1], |v0|, s86
	s_nop 1
	v_cndmask_b32_e64 v0, v10, v0, s[0:1]
	v_sub_f32_e32 v10, v7, v0
	v_add_f32_e32 v0, v6, v151
	v_min_f32_e32 v11, 0, v0
	v_mul_f32_e64 v0, |v0|, s81
; DI float log_sigmoid_f(float x) { return fminf(x, 0.f) - log1pf(__expf(-fabsf(x))); }
; DI float shup(float v, int o, int lane) { return __int_as_float(__builtin_amdgcn_ds_bpermute(((lane - o) & 63) << 2, __float_as_int(v))); }
; template <bool IS_MAX> DI void wscan2(float& x0, float& x1, int lane) {
;     x1 = IS_MAX ? fmaxf(x0, x1) : x0 + x1;
;     float s = x1;
; #pragma unroll
;     for (int o = 1; o < 64; o <<= 1) { const float y = shup(s, o, lane); if (lane >= o) s = IS_MAX ? fmaxf(s, y) : s + y; }
;     const float ex = shup(s, 1, lane);
;     if (lane > 0) { x0 = IS_MAX ? fmaxf(x0, ex) : x0 + ex; x1 = IS_MAX ? fmaxf(x1, ex) : x1 + ex; }
; }
; DI void ml_vectors(Frame& F, int l, int t0, int h, LAS float* A, LAS float* IG, LAS float* RED) {
;     ...
;         float a0 = log_sigmoid_f(gp[12 + h] + fb), a1 = log_sigmoid_f(gp[16 + 12 + h] + fb);
;         IG[s0] = gp[8 + h] + ib; IG[s0 + 1] = gp[16 + 8 + h] + ib;
;         wscan2<false>(a0, a1, F.lane);
;         A[s0] = a0; A[s0 + 1] = a1; }
	v_exp_f32_e32 v0, v0
	s_nop 0
	v_add_f32_e32 v20, 1.0, v0
	v_add_f32_e32 v6, -1.0, v20
	v_sub_f32_e32 v7, v6, v20
	v_add_f32_e32 v7, 1.0, v7
	v_sub_f32_e32 v6, v0, v6
	v_add_f32_e32 v21, v6, v7
	v_frexp_mant_f32_e32 v6, v20
	v_cmp_gt_f32_e64 s[0:1], s87, v6
	v_cvt_f64_f32_e32 v[6:7], v20
	v_frexp_exp_i32_f64_e32 v6, v[6:7]
	v_subbrev_co_u32_e64 v6, s[0:1], 0, v6, s[0:1]
	v_sub_u32_e32 v7, 0, v6
	v_ldexp_f32 v20, v20, v7
	v_ldexp_f32 v7, v21, v7
	v_add_f32_e32 v21, -1.0, v20
	v_add_f32_e32 v22, 1.0, v21
	v_sub_f32_e32 v22, v20, v22
	v_add_f32_e32 v22, v7, v22
	v_add_f32_e32 v23, v21, v22
	v_sub_f32_e32 v21, v23, v21
	v_sub_f32_e32 v21, v22, v21
	v_add_f32_e32 v22, 1.0, v20
	v_add_f32_e32 v28, -1.0, v22
	v_sub_f32_e32 v20, v20, v28
	v_add_f32_e32 v7, v7, v20
	v_add_f32_e32 v20, v22, v7
	v_sub_f32_e32 v22, v20, v22
	v_sub_f32_e32 v7, v7, v22
	v_rcp_f32_e32 v22, v20
	v_cvt_f32_i32_e32 v6, v6
	v_cmp_neq_f32_e64 s[0:1], s82, v0
	v_mul_f32_e32 v28, v23, v22
	v_mul_f32_e32 v29, v20, v28
	v_fma_f32 v30, v28, v20, -v29
	v_fmac_f32_e32 v30, v28, v7
	v_add_f32_e32 v31, v29, v30
	v_sub_f32_e32 v36, v23, v31
	v_sub_f32_e32 v23, v23, v36
	v_sub_f32_e32 v29, v31, v29
	v_sub_f32_e32 v23, v23, v31
	v_add_f32_e32 v21, v21, v23
	v_sub_f32_e32 v23, v29, v30
	v_add_f32_e32 v21, v23, v21
	v_add_f32_e32 v23, v36, v21
	v_mul_f32_e32 v29, v22, v23
	v_mul_f32_e32 v30, v20, v29
	v_fma_f32 v20, v29, v20, -v30
	v_fmac_f32_e32 v20, v29, v7
	v_sub_f32_e32 v7, v36, v23
	v_add_f32_e32 v7, v21, v7
	v_add_f32_e32 v21, v30, v20
	v_sub_f32_e32 v31, v23, v21
	v_sub_f32_e32 v23, v23, v31
	v_sub_f32_e32 v30, v21, v30
	v_sub_f32_e32 v21, v23, v21
	v_add_f32_e32 v7, v7, v21
	v_sub_f32_e32 v20, v30, v20
	v_add_f32_e32 v7, v20, v7
	v_add_f32_e32 v20, v28, v29
	v_add_f32_e32 v7, v31, v7
	v_sub_f32_e32 v21, v20, v28
	v_mul_f32_e32 v7, v22, v7
	v_sub_f32_e32 v21, v29, v21
	v_add_f32_e32 v7, v21, v7
	v_mul_f32_e32 v28, 0x3f317218, v6
	v_add_f32_e32 v21, v20, v7
	v_fma_f32 v29, v6, s80, -v28
	v_mul_f32_e32 v22, v21, v21
	v_fmac_f32_e32 v29, 0xb102e308, v6
	v_sub_f32_e32 v6, v21, v20
	v_fmamk_f32 v23, v22, 0x3e9b6dac, v216
	v_sub_f32_e32 v6, v7, v6
	v_add_f32_e32 v7, v28, v29
	v_fmaak_f32 v23, v22, v23, 0x3f2aaada
	v_sub_f32_e32 v20, v7, v28
	v_ldexp_f32 v28, v21, 1
	v_mul_f32_e32 v21, v21, v22
	v_mul_f32_e32 v21, v21, v23
	v_add_f32_e32 v22, v28, v21
	v_sub_f32_e32 v23, v22, v28
	v_ldexp_f32 v6, v6, 1
	v_sub_f32_e32 v21, v21, v23
	v_add_f32_e32 v6, v6, v21
	v_add_f32_e32 v21, v22, v6
	v_sub_f32_e32 v22, v21, v22
	v_sub_f32_e32 v6, v6, v22
	v_add_f32_e32 v22, v7, v21
	v_sub_f32_e32 v23, v22, v7
	v_sub_f32_e32 v28, v22, v23
	v_sub_f32_e32 v20, v29, v20
	v_sub_f32_e32 v7, v7, v28
	v_sub_f32_e32 v21, v21, v23
	v_add_f32_e32 v7, v21, v7
	v_add_f32_e32 v21, v20, v6
	v_sub_f32_e32 v23, v21, v20
	v_sub_f32_e32 v28, v21, v23
	v_sub_f32_e32 v20, v20, v28
	v_sub_f32_e32 v6, v6, v23
	v_add_f32_e32 v7, v21, v7
	v_add_f32_e32 v6, v6, v20
	v_add_f32_e32 v20, v22, v7
	v_sub_f32_e32 v21, v20, v22
	v_sub_f32_e32 v7, v7, v21
	v_add_f32_e32 v6, v6, v7
	v_add_f32_e32 v6, v20, v6
	v_cndmask_b32_e64 v6, v230, v6, s[0:1]
	v_cmp_ngt_f32_e64 s[0:1], -1.0, v0
	v_mov_b32_e32 v7, v152
	s_nop 0
	v_cndmask_b32_e64 v6, v231, v6, s[0:1]
	v_cmp_neq_f32_e64 s[0:1], -1.0, v0
	s_nop 1
	v_cndmask_b32_e64 v6, v232, v6, s[0:1]
	v_cmp_lt_f32_e64 s[0:1], |v0|, s86
	s_nop 1
	v_cndmask_b32_e64 v0, v6, v0, s[0:1]
	v_mov_b32_e32 v6, v153
	v_sub_f32_e32 v20, v11, v0
	v_lshl_add_u32 v11, v1, 3, s17
	v_add_u32_e32 v21, 0x9b00, v11
	v_add_f32_e32 v0, v10, v20
	v_cmp_gt_u32_e64 s[0:1], 2, v1
	s_waitcnt vmcnt(0)
	v_pk_add_f32 v[4:5], v[2:3], v[6:7] op_sel_hi:[0,1]
	v_add_u32_e32 v2, 0xfc, v9
	v_and_b32_e32 v2, 0xfc, v2
	ds_write2_b32 v21, v4, v5 offset1:1
	ds_bpermute_b32 v4, v2, v0
	v_add_u32_e32 v5, 0xf8, v9
	v_and_b32_e32 v5, 0xfc, v5
	s_waitcnt lgkmcnt(0)
	v_add_f32_e32 v4, v0, v4
	v_cndmask_b32_e32 v4, v4, v0, vcc
	ds_bpermute_b32 v5, v5, v4
	s_waitcnt lgkmcnt(0)
	v_add_f32_e32 v5, v4, v5
	v_cndmask_b32_e64 v4, v5, v4, s[0:1]
	v_add_u32_e32 v5, 0xf0, v9
	v_and_b32_e32 v5, 0xfc, v5
	ds_bpermute_b32 v5, v5, v4
	v_cmp_gt_u32_e64 s[0:1], 4, v1
	s_waitcnt lgkmcnt(0)
	v_add_f32_e32 v5, v4, v5
	v_cndmask_b32_e64 v4, v5, v4, s[0:1]
	v_add_u32_e32 v5, 0xe0, v9
	v_and_b32_e32 v5, 0xfc, v5
	ds_bpermute_b32 v5, v5, v4
	v_cmp_gt_u32_e64 s[0:1], 8, v1
	s_waitcnt lgkmcnt(0)
	v_add_f32_e32 v5, v4, v5
	v_cndmask_b32_e64 v4, v5, v4, s[0:1]
	v_add_u32_e32 v5, 0xc0, v9
	v_and_b32_e32 v5, 0xfc, v5
	ds_bpermute_b32 v5, v5, v4
	v_cmp_gt_u32_e64 s[0:1], 16, v1
	s_waitcnt lgkmcnt(0)
	v_add_f32_e32 v5, v4, v5
	v_cndmask_b32_e64 v4, v5, v4, s[0:1]
	ds_bpermute_b32 v5, v8, v4
	v_cmp_gt_u32_e64 s[0:1], 32, v1
	s_waitcnt lgkmcnt(0)
	v_add_f32_e32 v5, v4, v5
	v_cndmask_b32_e64 v4, v5, v4, s[0:1]
	ds_bpermute_b32 v2, v2, v4
	s_waitcnt lgkmcnt(0)
	v_add_f32_e32 v4, v10, v2
	v_add_f32_e32 v2, v0, v2
	v_cndmask_b32_e32 v4, v4, v10, vcc
	v_cndmask_b32_e32 v0, v2, v0, vcc
	v_add_u32_e32 v2, 0x9900, v11
	ds_write2_b32 v2, v4, v0 offset1:1

; #define LAS __attribute__((address_space(3)))
; DI float log_sigmoid_f(float x) { return fminf(x, 0.f) - log1pf(__expf(-fabsf(x))); }
; DI void ml_vectors(Frame& F, int l, int t0, int h, LAS float* A, LAS float* IG, LAS float* RED) {
;     (void)RED;
;     if (F.wave == 0) {
;         const int s0 = 2 * F.lane; const float* gp = (const float*)(F.ws + WS_GATES) + (size_t)(t0 + s0) * 16; const float fb = inp(F, I_FB)[l * 4 + h], ib = inp(F, I_IB)[l * 4 + h];
;         float a0 = log_sigmoid_f(gp[12 + h] + fb), a1 = log_sigmoid_f(gp[16 + 12 + h] + fb);
;         IG[s0] = gp[8 + h] + ib; IG[s0 + 1] = gp[16 + 8 + h] + ib;
; template <class Hook = NoHook> DI void ml_out_unit(Frame& F, int l, int ch, int h, const MlPre& P, Hook mid = Hook()) {
;     ...
;     const bf16* cin = (const bf16*)(F.ws + WS_MLC + ML_ALT(F.l) * (406 * MiB)) + (size_t)(ch * 4 + h) * 5120;
;     bf16x8 cb[2][5];
; #pragma unroll
;     for (int ks = 0; ks < 2; ++ks)
; #pragma unroll
;         for (int nt = 0; nt < 5; ++nt) { cb[ks][nt] = *(const bf16x8*)(cin + (16 * nt + (F.lane & 15)) * 64 + 32 * ks + 8 * (F.lane >> 4)); if (nt == 4 && (F.lane & 15) != 0) cb[ks][nt] = (bf16x8){0, 0, 0, 0, 0, 0, 0, 0}; }
;     ml_vectors(F, l, t0, h, A, IG, RED);
.LBB0_2858:
	s_or_b64 exec, exec, s[6:7]
	s_add_u32 s20, s20, s4
	s_addc_u32 s21, s21, s5
	s_add_i32 s1, s51, 0x1b500
	s_add_i32 s35, s51, 0x1b700
	s_lshl_b32 s28, s2, 7
	s_mul_i32 s2, s0, 0x2800
	s_mul_hi_i32 s3, s0, 0x2800
	s_add_u32 s2, s20, s2
	s_addc_u32 s3, s21, s3
	v_and_b32_e32 v2, 48, v130
	v_lshlrev_b32_e32 v4, 7, v130
	v_and_b32_e32 v45, 63, v130
	v_lshl_add_u64 v[0:1], s[2:3], 0, v[2:3]
	s_mov_b64 s[2:3], 0x23500000
	v_and_b32_e32 v22, 0x780, v4
	v_lshl_add_u64 v[20:21], v[0:1], 0, s[2:3]
	v_mov_b32_e32 v23, v3
	v_or_b32_e32 v26, 0x1000, v22
	v_mov_b32_e32 v27, v3
	v_lshl_or_b32 v16, v45, 7, v235
	v_mov_b32_e32 v17, v3
	v_or_b32_e32 v42, 0x2000, v22
	v_mov_b32_e32 v43, v3
	s_mov_b64 s[2:3], 0x23500040
	v_lshl_add_u64 v[24:25], v[20:21], 0, v[22:23]
	v_lshl_add_u64 v[12:13], v[20:21], 0, v[26:27]
	v_lshl_add_u64 v[40:41], v[20:21], 0, v[16:17]
	v_lshl_add_u64 v[20:21], v[20:21], 0, v[42:43]
	v_lshl_add_u64 v[0:1], v[0:1], 0, s[2:3]
	global_load_dwordx4 v[8:11], v[24:25], off
	global_load_dwordx4 v[4:7], v[24:25], off offset:2048
	global_load_dwordx4 v[36:39], v[20:21], off
	v_lshl_add_u64 v[20:21], v[0:1], 0, v[26:27]
	global_load_dwordx4 v[12:15], v[12:13], off
	v_lshl_add_u64 v[0:1], v[0:1], 0, v[42:43]
	global_load_dwordx4 v[16:19], v[40:41], off
	global_load_dwordx4 v[28:31], v[24:25], off offset:64
	global_load_dwordx4 v[32:35], v[24:25], off offset:2112
	s_nop 0
	global_load_dwordx4 v[24:27], v[20:21], off
	s_nop 0
	global_load_dwordx4 v[20:23], v[40:41], off offset:64
	s_cmp_lt_u32 s34, 64
	global_load_dwordx4 v[40:43], v[0:1], off
	s_cselect_b64 s[30:31], -1, 0
	v_lshlrev_b32_e32 v50, 3, v45
	v_lshlrev_b32_e32 v1, 2, v45
	s_and_b64 vcc, exec, s[30:31]
	v_cmp_eq_u32_e64 s[2:3], 0, v45
	v_cmp_gt_u32_e64 s[12:13], 2, v45
	v_cmp_gt_u32_e64 s[10:11], 4, v45
	v_cmp_gt_u32_e64 s[8:9], 8, v45
	v_cmp_gt_u32_e64 s[6:7], 16, v45
	v_cmp_gt_u32_e64 s[4:5], 32, v45
	v_add_u32_e32 v51, s35, v50
	v_add_u32_e32 v57, 0xfc, v1
	v_add_u32_e32 v56, 0xf8, v1
	v_add_u32_e32 v55, 0xf0, v1
	v_add_u32_e32 v54, 0xe0, v1
	v_add_u32_e32 v53, 0xc0, v1
	v_xor_b32_e32 v52, 0x80, v1
	v_add_u32_e32 v58, s1, v50
	s_cbranch_vccz .LBB0_2860
	s_add_i32 s1, s51, 0x20870
	v_mov_b32_e32 v0, s1
	ds_read2_b32 v[48:49], v0 offset1:1
	s_or_b32 s38, s29, s22
	s_ashr_i32 s39, s38, 31
	s_lshl_b64 s[38:39], s[38:39], 2
	v_lshl_or_b32 v46, v45, 1, s28
	s_waitcnt lgkmcnt(0)
	v_readfirstlane_b32 s1, v48
	v_readfirstlane_b32 s37, v49
	s_add_u32 s40, s1, s38
	s_addc_u32 s41, s37, s39
	s_add_i32 s1, s51, 0x20868
	v_mov_b32_e32 v0, s1
	ds_read2_b32 v[60:61], v0 offset1:1
	v_ashrrev_i32_e32 v47, 31, v46
	v_lshlrev_b64 v[46:47], 6, v[46:47]
	v_lshl_add_u64 v[46:47], s[20:21], 0, v[46:47]
	global_load_dword v48, v3, s[40:41]
	s_waitcnt lgkmcnt(0)
	v_readfirstlane_b32 s1, v60
	v_readfirstlane_b32 s37, v61
	s_add_u32 s38, s1, s38
	s_addc_u32 s39, s37, s39
	s_lshl_b32 s52, s29, 2
	global_load_dword v44, v3, s[38:39]
	v_lshl_add_u64 v[46:47], v[46:47], 0, s[52:53]
	s_mov_b64 s[38:39], 0x500000
	v_lshl_add_u64 v[46:47], v[46:47], 0, s[38:39]
	global_load_dword v0, v[46:47], off offset:48
	global_load_dword v152, v[46:47], off offset:32
	global_load_dword v153, v[46:47], off offset:96
	global_load_dword v151, v[46:47], off offset:112
	s_waitcnt vmcnt(0)
	v_add_f32_e32 v0, v48, v0
	v_min_f32_e32 v49, 0, v0
	v_mul_f32_e64 v0, |v0|, s81
	v_exp_f32_e32 v0, v0
	s_nop 0
	v_add_f32_e32 v59, 1.0, v0
	v_add_f32_e32 v60, -1.0, v59
	v_sub_f32_e32 v61, v60, v59
	v_add_f32_e32 v61, 1.0, v61
	v_sub_f32_e32 v60, v0, v60
	v_add_f32_e32 v62, v60, v61
	v_frexp_mant_f32_e32 v60, v59
	v_cmp_gt_f32_e32 vcc, s87, v60
	v_cvt_f64_f32_e32 v[60:61], v59
	v_frexp_exp_i32_f64_e32 v60, v[60:61]
	v_subbrev_co_u32_e32 v60, vcc, 0, v60, vcc
	v_sub_u32_e32 v61, 0, v60
	v_ldexp_f32 v59, v59, v61
	v_ldexp_f32 v61, v62, v61
	v_add_f32_e32 v62, -1.0, v59
	v_add_f32_e32 v63, 1.0, v62
	v_sub_f32_e32 v63, v59, v63
	v_add_f32_e32 v63, v61, v63
	v_add_f32_e32 v64, v62, v63
	v_sub_f32_e32 v62, v64, v62
	v_sub_f32_e32 v62, v63, v62
	v_add_f32_e32 v63, 1.0, v59
	v_add_f32_e32 v65, -1.0, v63
	v_sub_f32_e32 v59, v59, v65
	v_add_f32_e32 v59, v61, v59
	v_add_f32_e32 v61, v63, v59
	v_sub_f32_e32 v63, v61, v63
	v_sub_f32_e32 v59, v59, v63
	v_rcp_f32_e32 v63, v61
	v_cvt_f32_i32_e32 v60, v60
	v_cmp_neq_f32_e32 vcc, s82, v0
	v_mul_f32_e32 v65, v64, v63
	v_mul_f32_e32 v66, v61, v65
	v_fma_f32 v67, v65, v61, -v66
	v_fmac_f32_e32 v67, v65, v59
	v_add_f32_e32 v68, v66, v67
	v_sub_f32_e32 v69, v64, v68
	v_sub_f32_e32 v64, v64, v69
	v_sub_f32_e32 v66, v68, v66
	v_sub_f32_e32 v64, v64, v68
	v_add_f32_e32 v62, v62, v64
	v_sub_f32_e32 v64, v66, v67
	v_add_f32_e32 v62, v64, v62
	v_add_f32_e32 v64, v69, v62
	v_mul_f32_e32 v66, v63, v64
	v_mul_f32_e32 v67, v61, v66
	v_fma_f32 v61, v66, v61, -v67
	v_fmac_f32_e32 v61, v66, v59
	v_sub_f32_e32 v59, v69, v64
	v_add_f32_e32 v59, v62, v59
	v_add_f32_e32 v62, v67, v61
	v_sub_f32_e32 v68, v64, v62
	v_sub_f32_e32 v64, v64, v68
	v_sub_f32_e32 v67, v62, v67
	v_sub_f32_e32 v62, v64, v62
	v_add_f32_e32 v59, v59, v62
	v_sub_f32_e32 v61, v67, v61
	v_add_f32_e32 v59, v61, v59
	v_add_f32_e32 v61, v65, v66
	v_add_f32_e32 v59, v68, v59
	v_sub_f32_e32 v62, v61, v65
	v_mul_f32_e32 v59, v63, v59
	v_sub_f32_e32 v62, v66, v62
	v_add_f32_e32 v59, v62, v59
	v_mul_f32_e32 v65, 0x3f317218, v60
	v_add_f32_e32 v62, v61, v59
	v_fma_f32 v66, v60, s80, -v65
	v_mul_f32_e32 v63, v62, v62
	v_fmac_f32_e32 v66, 0xb102e308, v60
	v_sub_f32_e32 v60, v62, v61
	v_fmamk_f32 v64, v63, 0x3e9b6dac, v216
	v_sub_f32_e32 v59, v59, v60
	v_add_f32_e32 v60, v65, v66
	v_fmaak_f32 v64, v63, v64, 0x3f2aaada
	v_sub_f32_e32 v61, v60, v65
	v_ldexp_f32 v65, v62, 1
; DI float log_sigmoid_f(float x) { return fminf(x, 0.f) - log1pf(__expf(-fabsf(x))); }
; DI float shup(float v, int o, int lane) { return __int_as_float(__builtin_amdgcn_ds_bpermute(((lane - o) & 63) << 2, __float_as_int(v))); }
; template <bool IS_MAX> DI void wscan2(float& x0, float& x1, int lane) {
;     x1 = IS_MAX ? fmaxf(x0, x1) : x0 + x1;
;     float s = x1;
; #pragma unroll
;     for (int o = 1; o < 64; o <<= 1) { const float y = shup(s, o, lane); if (lane >= o) s = IS_MAX ? fmaxf(s, y) : s + y; }
;     const float ex = shup(s, 1, lane);
;     if (lane > 0) { x0 = IS_MAX ? fmaxf(x0, ex) : x0 + ex; x1 = IS_MAX ? fmaxf(x1, ex) : x1 + ex; }
; }
; DI void ml_vectors(Frame& F, int l, int t0, int h, LAS float* A, LAS float* IG, LAS float* RED) {
;     ...
;         float a0 = log_sigmoid_f(gp[12 + h] + fb), a1 = log_sigmoid_f(gp[16 + 12 + h] + fb);
;         IG[s0] = gp[8 + h] + ib; IG[s0 + 1] = gp[16 + 8 + h] + ib;
;         wscan2<false>(a0, a1, F.lane);
;         A[s0] = a0; A[s0 + 1] = a1; }
	v_mul_f32_e32 v62, v62, v63
	v_mul_f32_e32 v62, v62, v64
	v_add_f32_e32 v63, v65, v62
	v_sub_f32_e32 v64, v63, v65
	v_ldexp_f32 v59, v59, 1
	v_sub_f32_e32 v62, v62, v64
	v_add_f32_e32 v59, v59, v62
	v_add_f32_e32 v62, v63, v59
	v_sub_f32_e32 v63, v62, v63
	v_sub_f32_e32 v59, v59, v63
	v_add_f32_e32 v63, v60, v62
	v_sub_f32_e32 v64, v63, v60
	v_sub_f32_e32 v65, v63, v64
	v_sub_f32_e32 v61, v66, v61
	v_sub_f32_e32 v60, v60, v65
	v_sub_f32_e32 v62, v62, v64
	v_add_f32_e32 v60, v62, v60
	v_add_f32_e32 v62, v61, v59
	v_sub_f32_e32 v64, v62, v61
	v_sub_f32_e32 v65, v62, v64
	v_sub_f32_e32 v61, v61, v65
	v_sub_f32_e32 v59, v59, v64
	v_add_f32_e32 v60, v62, v60
	v_add_f32_e32 v59, v59, v61
	v_add_f32_e32 v61, v63, v60
	v_sub_f32_e32 v62, v61, v63
	v_sub_f32_e32 v60, v60, v62
	v_add_f32_e32 v59, v59, v60
	v_add_f32_e32 v59, v61, v59
	v_cndmask_b32_e32 v59, v230, v59, vcc
	v_cmp_ngt_f32_e32 vcc, -1.0, v0
	s_nop 1
	v_cndmask_b32_e32 v59, v231, v59, vcc
	v_cmp_neq_f32_e32 vcc, -1.0, v0
	s_nop 1
	v_cndmask_b32_e32 v59, v232, v59, vcc
	v_cmp_lt_f32_e64 vcc, |v0|, s86
	s_nop 1
	v_cndmask_b32_e32 v0, v59, v0, vcc
	v_sub_f32_e32 v59, v49, v0
	v_add_f32_e32 v0, v48, v151
	v_min_f32_e32 v60, 0, v0
	v_mul_f32_e64 v0, |v0|, s81
	v_exp_f32_e32 v0, v0
	s_nop 0
	v_add_f32_e32 v61, 1.0, v0
	v_add_f32_e32 v48, -1.0, v61
	v_sub_f32_e32 v49, v48, v61
	v_add_f32_e32 v49, 1.0, v49
	v_sub_f32_e32 v48, v0, v48
	v_add_f32_e32 v62, v48, v49
	v_frexp_mant_f32_e32 v48, v61
	v_cmp_gt_f32_e32 vcc, s87, v48
	v_cvt_f64_f32_e32 v[48:49], v61
	v_frexp_exp_i32_f64_e32 v48, v[48:49]
	v_subbrev_co_u32_e32 v48, vcc, 0, v48, vcc
	v_sub_u32_e32 v49, 0, v48
	v_ldexp_f32 v61, v61, v49
	v_ldexp_f32 v49, v62, v49
	v_add_f32_e32 v62, -1.0, v61
	v_add_f32_e32 v63, 1.0, v62
	v_sub_f32_e32 v63, v61, v63
	v_add_f32_e32 v63, v49, v63
	v_add_f32_e32 v64, v62, v63
	v_sub_f32_e32 v62, v64, v62
	v_sub_f32_e32 v62, v63, v62
	v_add_f32_e32 v63, 1.0, v61
	v_add_f32_e32 v65, -1.0, v63
	v_sub_f32_e32 v61, v61, v65
	v_add_f32_e32 v49, v49, v61
	v_add_f32_e32 v61, v63, v49
	v_sub_f32_e32 v63, v61, v63
	v_sub_f32_e32 v49, v49, v63
	v_rcp_f32_e32 v63, v61
	v_cvt_f32_i32_e32 v48, v48
	v_cmp_neq_f32_e32 vcc, s82, v0
	v_mul_f32_e32 v65, v64, v63
	v_mul_f32_e32 v66, v61, v65
	v_fma_f32 v67, v65, v61, -v66
	v_fmac_f32_e32 v67, v65, v49
	v_add_f32_e32 v68, v66, v67
	v_sub_f32_e32 v69, v64, v68
	v_sub_f32_e32 v64, v64, v69
	v_sub_f32_e32 v66, v68, v66
	v_sub_f32_e32 v64, v64, v68
	v_add_f32_e32 v62, v62, v64
	v_sub_f32_e32 v64, v66, v67
	v_add_f32_e32 v62, v64, v62
	v_add_f32_e32 v64, v69, v62
	v_mul_f32_e32 v66, v63, v64
	v_mul_f32_e32 v67, v61, v66
	v_fma_f32 v61, v66, v61, -v67
	v_fmac_f32_e32 v61, v66, v49
	v_sub_f32_e32 v49, v69, v64
	v_add_f32_e32 v49, v62, v49
	v_add_f32_e32 v62, v67, v61
	v_sub_f32_e32 v68, v64, v62
	v_sub_f32_e32 v64, v64, v68
	v_sub_f32_e32 v67, v62, v67
	v_sub_f32_e32 v62, v64, v62
	v_add_f32_e32 v49, v49, v62
	v_sub_f32_e32 v61, v67, v61
	v_add_f32_e32 v49, v61, v49
	v_add_f32_e32 v61, v65, v66
	v_add_f32_e32 v49, v68, v49
	v_sub_f32_e32 v62, v61, v65
	v_mul_f32_e32 v49, v63, v49
	v_sub_f32_e32 v62, v66, v62
	v_add_f32_e32 v49, v62, v49
	v_mul_f32_e32 v65, 0x3f317218, v48
	v_add_f32_e32 v62, v61, v49
	v_fma_f32 v66, v48, s80, -v65
	v_mul_f32_e32 v63, v62, v62
	v_fmac_f32_e32 v66, 0xb102e308, v48
	v_sub_f32_e32 v48, v62, v61
	v_fmamk_f32 v64, v63, 0x3e9b6dac, v216
	v_sub_f32_e32 v48, v49, v48
	v_add_f32_e32 v49, v65, v66
	v_fmaak_f32 v64, v63, v64, 0x3f2aaada
	v_sub_f32_e32 v61, v49, v65
	v_ldexp_f32 v65, v62, 1
	v_mul_f32_e32 v62, v62, v63
	v_mul_f32_e32 v62, v62, v64
	v_add_f32_e32 v63, v65, v62
	v_sub_f32_e32 v64, v63, v65
	v_ldexp_f32 v48, v48, 1
	v_sub_f32_e32 v62, v62, v64
	v_add_f32_e32 v48, v48, v62
	v_add_f32_e32 v62, v63, v48
	v_sub_f32_e32 v63, v62, v63
	v_sub_f32_e32 v48, v48, v63
	v_add_f32_e32 v63, v49, v62
	v_sub_f32_e32 v64, v63, v49
	v_sub_f32_e32 v65, v63, v64
	v_sub_f32_e32 v61, v66, v61
	v_sub_f32_e32 v49, v49, v65
	v_sub_f32_e32 v62, v62, v64
	v_add_f32_e32 v49, v62, v49
	v_add_f32_e32 v62, v61, v48
	v_sub_f32_e32 v64, v62, v61
	v_sub_f32_e32 v65, v62, v64
	v_sub_f32_e32 v61, v61, v65
	v_sub_f32_e32 v48, v48, v64
	v_add_f32_e32 v49, v62, v49
	v_add_f32_e32 v48, v48, v61
	v_add_f32_e32 v61, v63, v49
	v_sub_f32_e32 v62, v61, v63
	v_sub_f32_e32 v49, v49, v62
	v_add_f32_e32 v48, v48, v49
	v_add_f32_e32 v48, v61, v48
	v_cndmask_b32_e32 v48, v230, v48, vcc
	v_cmp_ngt_f32_e32 vcc, -1.0, v0
	s_nop 1
	v_cndmask_b32_e32 v48, v231, v48, vcc
	v_cmp_neq_f32_e32 vcc, -1.0, v0
	s_nop 1
	v_cndmask_b32_e32 v48, v232, v48, vcc
	v_cmp_lt_f32_e64 vcc, |v0|, s86
	s_nop 1
	v_cndmask_b32_e32 v0, v48, v0, vcc
	v_mov_b32_e32 v48, v152
	v_mov_b32_e32 v49, v153
	v_sub_f32_e32 v60, v60, v0
	v_add_f32_e32 v0, v59, v60
	s_waitcnt vmcnt(0)
	v_pk_add_f32 v[46:47], v[44:45], v[48:49] op_sel_hi:[0,1]
	v_and_b32_e32 v44, 0xfc, v57
	ds_write2_b32 v51, v46, v47 offset1:1
	ds_bpermute_b32 v46, v44, v0
	v_and_b32_e32 v47, 0xfc, v56
	s_waitcnt lgkmcnt(0)
	v_add_f32_e32 v46, v0, v46
	v_cndmask_b32_e64 v46, v46, v0, s[2:3]
	ds_bpermute_b32 v47, v47, v46
	s_waitcnt lgkmcnt(0)
	v_add_f32_e32 v47, v46, v47
	v_cndmask_b32_e64 v46, v47, v46, s[12:13]
	v_and_b32_e32 v47, 0xfc, v55
	ds_bpermute_b32 v47, v47, v46
	s_waitcnt lgkmcnt(0)
	v_add_f32_e32 v47, v46, v47
	v_cndmask_b32_e64 v46, v47, v46, s[10:11]
	v_and_b32_e32 v47, 0xfc, v54
	ds_bpermute_b32 v47, v47, v46
	s_waitcnt lgkmcnt(0)
	v_add_f32_e32 v47, v46, v47
	v_cndmask_b32_e64 v46, v47, v46, s[8:9]
	v_and_b32_e32 v47, 0xfc, v53
	ds_bpermute_b32 v47, v47, v46
	s_waitcnt lgkmcnt(0)
	v_add_f32_e32 v47, v46, v47
	v_cndmask_b32_e64 v46, v47, v46, s[6:7]
	ds_bpermute_b32 v47, v52, v46
	s_waitcnt lgkmcnt(0)
	v_add_f32_e32 v47, v46, v47
	v_cndmask_b32_e64 v46, v47, v46, s[4:5]
	ds_bpermute_b32 v44, v44, v46
	s_waitcnt lgkmcnt(0)
	v_add_f32_e32 v46, v59, v44
	v_add_f32_e32 v44, v0, v44
	v_cndmask_b32_e64 v46, v46, v59, s[2:3]
	v_cndmask_b32_e64 v0, v44, v0, s[2:3]
	ds_write2_b32 v58, v46, v0 offset1:1
